# cfgN + non-temporal hint on the stores of the late-consumed dense weight conversions (w_out1, w_glu, w_in1, FFN weights)
# baseline (speedup 1.0000x reference)
.LBB0_17:
	s_or_b64 exec, exec, s[12:13]
	s_waitcnt vmcnt(0)
	ds_write2_b32 v73, v6, v7 offset1:1
	ds_write2_b32 v73, v8, v9 offset0:2 offset1:3
	v_add_u32_e32 v6, 0x410, v73
	ds_write2_b32 v6, v2, v3 offset1:1
	v_add_u32_e32 v2, 0x418, v73
	ds_write2_b32 v2, v4, v5 offset1:1
	v_add_u32_e32 v2, 0x820, v73
	ds_write2_b32 v2, v14, v15 offset1:1
	v_add_u32_e32 v2, 0x828, v73
	ds_write2_b32 v2, v16, v17 offset1:1
	v_add_u32_e32 v2, 0xc30, v73
	ds_write2_b32 v2, v10, v11 offset1:1
	v_add_u32_e32 v2, 0xc38, v73
	ds_write2_b32 v2, v12, v13 offset1:1
	v_add_u32_e32 v2, 0x1040, v73
	ds_write2_b32 v2, v22, v23 offset1:1
	v_add_u32_e32 v2, 0x1048, v73
	ds_write2_b32 v2, v24, v25 offset1:1
	v_add_u32_e32 v2, 0x1450, v73
	ds_write2_b32 v2, v18, v19 offset1:1
	v_add_u32_e32 v2, 0x1458, v73
	ds_write2_b32 v2, v20, v21 offset1:1
	v_add_u32_e32 v2, 0x1860, v73
	ds_write2_b32 v2, v30, v31 offset1:1
	v_add_u32_e32 v2, 0x1868, v73
	ds_write2_b32 v2, v32, v33 offset1:1
	v_add_u32_e32 v2, 0x1c70, v73
	ds_write2_b32 v2, v26, v27 offset1:1
	v_add_u32_e32 v2, 0x1c78, v73
	ds_write2_b32 v2, v28, v29 offset1:1
	v_add_u32_e32 v2, 0x2080, v73
	ds_write2_b32 v2, v38, v39 offset1:1
	v_add_u32_e32 v2, 0x2088, v73
	ds_write2_b32 v2, v40, v41 offset1:1
	v_add_u32_e32 v2, 0x2490, v73
	ds_write2_b32 v2, v34, v35 offset1:1
	v_add_u32_e32 v2, 0x2498, v73
	ds_write2_b32 v2, v36, v37 offset1:1
	v_add_u32_e32 v2, 0x28a0, v73
	ds_write2_b32 v2, v46, v47 offset1:1
	v_add_u32_e32 v2, 0x28a8, v73
	ds_write2_b32 v2, v48, v49 offset1:1
	v_add_u32_e32 v2, 0x2cb0, v73
	ds_write2_b32 v2, v42, v43 offset1:1
	v_add_u32_e32 v2, 0x2cb8, v73
	ds_write2_b32 v2, v44, v45 offset1:1
	v_add_u32_e32 v2, 0x30c0, v73
	ds_write2_b32 v2, v54, v55 offset1:1
	v_add_u32_e32 v2, 0x30c8, v73
	ds_write2_b32 v2, v56, v57 offset1:1
	v_add_u32_e32 v2, 0x34d0, v73
	ds_write2_b32 v2, v50, v51 offset1:1
	v_add_u32_e32 v2, 0x34d8, v73
	ds_write2_b32 v2, v52, v53 offset1:1
	v_add_u32_e32 v2, 0x38e0, v73
	ds_write2_b32 v2, v62, v63 offset1:1
	v_add_u32_e32 v2, 0x38e8, v73
	ds_write2_b32 v2, v64, v65 offset1:1
	v_add_u32_e32 v2, 0x3cf0, v73
	ds_write2_b32 v2, v58, v59 offset1:1
	v_add_u32_e32 v2, 0x3cf8, v73
	ds_write2_b32 v2, v60, v61 offset1:1
	s_waitcnt lgkmcnt(0)
	v_add_u32_e32 v26, 0x400, v88
	ds_read2_b32 v[6:7], v88 offset0:65 offset1:73
	ds_read2_b32 v[8:9], v88 offset1:8
	ds_read2_b32 v[10:11], v88 offset0:130 offset1:138
	ds_read2_b32 v[12:13], v88 offset0:195 offset1:203
	ds_read2_b32 v[16:17], v26 offset0:4 offset1:12
	ds_read2_b32 v[18:19], v26 offset0:69 offset1:77
	ds_read2_b32 v[20:21], v26 offset0:134 offset1:142
	ds_read2_b32 v[22:23], v26 offset0:199 offset1:207
	v_sub_u32_e32 v84, 0, v97
	v_add_u32_e32 v86, v77, v84
	v_ashrrev_i32_e32 v85, 31, v96
	v_ashrrev_i32_e32 v87, 31, v86
	s_waitcnt lgkmcnt(6)
	v_cvt_pk_f16_f32 v2, v8, v6
	s_waitcnt lgkmcnt(4)
	v_cvt_pk_f16_f32 v3, v10, v12
	s_waitcnt lgkmcnt(2)
	v_cvt_pk_f16_f32 v4, v16, v18
	s_waitcnt lgkmcnt(0)
	v_cvt_pk_f16_f32 v5, v20, v22
	v_or_b32_e32 v84, v96, v66
	v_lshl_add_u64 v[14:15], v[86:87], 1, v[82:83]
	v_add_u32_e32 v2, 0x80008, v2
	v_add_u32_e32 v3, 0x80008, v3
	v_add_u32_e32 v4, 0x80008, v4
	v_add_u32_e32 v5, 0x80008, v5
	v_lshlrev_b64 v[24:25], 12, v[84:85]
	v_and_b32_e32 v2, 0xfff0fff0, v2
	v_and_b32_e32 v3, 0xfff0fff0, v3
	v_and_b32_e32 v4, 0xfff0fff0, v4
	v_and_b32_e32 v5, 0xfff0fff0, v5
	v_lshl_add_u64 v[24:25], v[14:15], 0, v[24:25]
	global_store_dwordx4 v[24:25], v[2:5], off nt
	v_or_b32_e32 v84, v96, v68
	v_add_u32_e32 v95, s3, v95
	v_cvt_pk_f16_f32 v2, v9, v7
	v_cvt_pk_f16_f32 v3, v11, v13
	v_cvt_pk_f16_f32 v4, v17, v19
	v_cvt_pk_f16_f32 v5, v21, v23
	v_add_u32_e32 v2, 0x80008, v2
	v_add_u32_e32 v3, 0x80008, v3
	v_add_u32_e32 v4, 0x80008, v4
	v_add_u32_e32 v5, 0x80008, v5
	v_lshlrev_b64 v[6:7], 12, v[84:85]
	v_and_b32_e32 v2, 0xfff0fff0, v2
	v_and_b32_e32 v3, 0xfff0fff0, v3
	v_and_b32_e32 v4, 0xfff0fff0, v4
	v_and_b32_e32 v5, 0xfff0fff0, v5
	v_lshl_add_u64 v[6:7], v[14:15], 0, v[6:7]
	ds_read2_b32 v[8:9], v88 offset0:81 offset1:89
	ds_read2_b32 v[10:11], v88 offset0:16 offset1:24
	ds_read2_b32 v[12:13], v88 offset0:146 offset1:154
	ds_read2_b32 v[16:17], v88 offset0:211 offset1:219
	global_store_dwordx4 v[6:7], v[2:5], off nt
	ds_read2_b32 v[6:7], v26 offset0:20 offset1:28
	ds_read2_b32 v[18:19], v26 offset0:85 offset1:93
	ds_read2_b32 v[20:21], v26 offset0:150 offset1:158
	ds_read2_b32 v[22:23], v26 offset0:215 offset1:223
	s_waitcnt lgkmcnt(6)
	v_cvt_pk_f16_f32 v2, v10, v8
	s_waitcnt lgkmcnt(4)
	v_cvt_pk_f16_f32 v3, v12, v16
	v_or_b32_e32 v84, v96, v70
	s_waitcnt lgkmcnt(2)
	v_cvt_pk_f16_f32 v4, v6, v18
	s_waitcnt lgkmcnt(0)
	v_cvt_pk_f16_f32 v5, v20, v22
	v_add_u32_e32 v2, 0x80008, v2
	v_add_u32_e32 v3, 0x80008, v3
	v_add_u32_e32 v4, 0x80008, v4
	v_add_u32_e32 v5, 0x80008, v5
	v_lshlrev_b64 v[24:25], 12, v[84:85]
	v_and_b32_e32 v2, 0xfff0fff0, v2
	v_and_b32_e32 v3, 0xfff0fff0, v3
	v_and_b32_e32 v4, 0xfff0fff0, v4
	v_and_b32_e32 v5, 0xfff0fff0, v5
	v_lshl_add_u64 v[24:25], v[14:15], 0, v[24:25]
	global_store_dwordx4 v[24:25], v[2:5], off nt
	v_or_b32_e32 v84, v96, v72
	v_cmp_lt_i32_e32 vcc, s16, v95
	v_cvt_pk_f16_f32 v2, v11, v9
	v_cvt_pk_f16_f32 v3, v13, v17
	v_cvt_pk_f16_f32 v4, v7, v19
	v_cvt_pk_f16_f32 v5, v21, v23
	v_add_u32_e32 v2, 0x80008, v2
	v_add_u32_e32 v3, 0x80008, v3
	v_add_u32_e32 v4, 0x80008, v4
	v_add_u32_e32 v5, 0x80008, v5
	v_lshlrev_b64 v[6:7], 12, v[84:85]
	v_and_b32_e32 v2, 0xfff0fff0, v2
	v_and_b32_e32 v3, 0xfff0fff0, v3
	v_and_b32_e32 v4, 0xfff0fff0, v4
	v_and_b32_e32 v5, 0xfff0fff0, v5
	v_lshl_add_u64 v[6:7], v[14:15], 0, v[6:7]
	ds_read2_b32 v[8:9], v88 offset0:32 offset1:40
	ds_read2_b32 v[10:11], v88 offset0:97 offset1:105
	ds_read2_b32 v[12:13], v88 offset0:162 offset1:170
	ds_read2_b32 v[16:17], v88 offset0:227 offset1:235
	global_store_dwordx4 v[6:7], v[2:5], off nt
	ds_read2_b32 v[6:7], v26 offset0:36 offset1:44
	ds_read2_b32 v[18:19], v26 offset0:101 offset1:109
	ds_read2_b32 v[20:21], v26 offset0:166 offset1:174
	ds_read2_b32 v[22:23], v26 offset0:231 offset1:239
	s_waitcnt lgkmcnt(6)
	v_cvt_pk_f16_f32 v2, v8, v10
	s_waitcnt lgkmcnt(4)
	v_cvt_pk_f16_f32 v3, v12, v16
	v_or_b32_e32 v84, v96, v89
	s_waitcnt lgkmcnt(2)
	v_cvt_pk_f16_f32 v4, v6, v18
	s_waitcnt lgkmcnt(0)
	v_cvt_pk_f16_f32 v5, v20, v22
	v_add_u32_e32 v2, 0x80008, v2
	v_add_u32_e32 v3, 0x80008, v3
	v_add_u32_e32 v4, 0x80008, v4
	v_add_u32_e32 v5, 0x80008, v5
	v_lshlrev_b64 v[24:25], 12, v[84:85]
	v_and_b32_e32 v2, 0xfff0fff0, v2
	v_and_b32_e32 v3, 0xfff0fff0, v3
	v_and_b32_e32 v4, 0xfff0fff0, v4
	v_and_b32_e32 v5, 0xfff0fff0, v5
	v_lshl_add_u64 v[24:25], v[14:15], 0, v[24:25]
	global_store_dwordx4 v[24:25], v[2:5], off nt
	v_or_b32_e32 v84, v96, v90
	s_or_b64 s[8:9], vcc, s[8:9]
	v_cvt_pk_f16_f32 v2, v9, v11
	v_cvt_pk_f16_f32 v3, v13, v17
	v_cvt_pk_f16_f32 v4, v7, v19
	v_cvt_pk_f16_f32 v5, v21, v23
	v_add_u32_e32 v2, 0x80008, v2
	v_add_u32_e32 v3, 0x80008, v3
	v_add_u32_e32 v4, 0x80008, v4
	v_add_u32_e32 v5, 0x80008, v5
	v_lshlrev_b64 v[6:7], 12, v[84:85]
	v_and_b32_e32 v2, 0xfff0fff0, v2
	v_and_b32_e32 v3, 0xfff0fff0, v3
	v_and_b32_e32 v4, 0xfff0fff0, v4
	v_and_b32_e32 v5, 0xfff0fff0, v5
	v_lshl_add_u64 v[6:7], v[14:15], 0, v[6:7]
	ds_read2_b32 v[8:9], v88 offset0:48 offset1:56
	ds_read2_b32 v[10:11], v88 offset0:113 offset1:121
	ds_read2_b32 v[12:13], v88 offset0:178 offset1:186
	ds_read2_b32 v[16:17], v88 offset0:243 offset1:251
	global_store_dwordx4 v[6:7], v[2:5], off nt
	ds_read2_b32 v[6:7], v26 offset0:52 offset1:60
	ds_read2_b32 v[18:19], v26 offset0:117 offset1:125
	ds_read2_b32 v[20:21], v26 offset0:182 offset1:190
	ds_read2_b32 v[22:23], v26 offset0:247 offset1:255
	s_waitcnt lgkmcnt(6)
	v_cvt_pk_f16_f32 v2, v8, v10
	s_waitcnt lgkmcnt(4)
	v_cvt_pk_f16_f32 v3, v12, v16
	v_or_b32_e32 v84, v96, v91
	s_waitcnt lgkmcnt(2)
	v_cvt_pk_f16_f32 v4, v6, v18
	s_waitcnt lgkmcnt(0)
	v_cvt_pk_f16_f32 v5, v20, v22
	v_add_u32_e32 v2, 0x80008, v2
	v_add_u32_e32 v3, 0x80008, v3
	v_add_u32_e32 v4, 0x80008, v4
	v_add_u32_e32 v5, 0x80008, v5
	v_lshlrev_b64 v[24:25], 12, v[84:85]
	v_and_b32_e32 v2, 0xfff0fff0, v2
	v_and_b32_e32 v3, 0xfff0fff0, v3
	v_and_b32_e32 v4, 0xfff0fff0, v4
	v_and_b32_e32 v5, 0xfff0fff0, v5
	v_lshl_add_u64 v[24:25], v[14:15], 0, v[24:25]
	global_store_dwordx4 v[24:25], v[2:5], off nt
	v_or_b32_e32 v84, v96, v92
	v_add_u32_e32 v77, s14, v77
	v_cvt_pk_f16_f32 v2, v9, v11
	v_cvt_pk_f16_f32 v3, v13, v17
	v_cvt_pk_f16_f32 v4, v7, v19
	v_cvt_pk_f16_f32 v5, v21, v23
	v_add_u32_e32 v2, 0x80008, v2
	v_add_u32_e32 v3, 0x80008, v3
	v_add_u32_e32 v4, 0x80008, v4
	v_add_u32_e32 v5, 0x80008, v5
	v_lshlrev_b64 v[6:7], 12, v[84:85]
	v_and_b32_e32 v2, 0xfff0fff0, v2
	v_and_b32_e32 v3, 0xfff0fff0, v3
	v_and_b32_e32 v4, 0xfff0fff0, v4
	v_and_b32_e32 v5, 0xfff0fff0, v5
	v_lshl_add_u64 v[6:7], v[14:15], 0, v[6:7]
	global_store_dwordx4 v[6:7], v[2:5], off nt
	s_waitcnt lgkmcnt(0)
	s_andn2_b64 exec, exec, s[8:9]
	s_cbranch_execz .LBB0_50

.LBB0_52:
	s_or_b64 exec, exec, s[12:13]
	s_waitcnt vmcnt(0)
	ds_write2_b32 v73, v2, v3 offset1:1
	ds_write2_b32 v73, v4, v5 offset0:2 offset1:3
	v_add_u32_e32 v2, 0x410, v73
	ds_write2_b32 v2, v10, v11 offset1:1
	v_add_u32_e32 v2, 0x418, v73
	ds_write2_b32 v2, v12, v13 offset1:1
	v_add_u32_e32 v2, 0x820, v73
	ds_write2_b32 v2, v6, v7 offset1:1
	v_add_u32_e32 v2, 0x828, v73
	ds_write2_b32 v2, v8, v9 offset1:1
	v_add_u32_e32 v2, 0xc30, v73
	ds_write2_b32 v2, v18, v19 offset1:1
	v_add_u32_e32 v2, 0xc38, v73
	ds_write2_b32 v2, v20, v21 offset1:1
	v_add_u32_e32 v2, 0x1040, v73
	ds_write2_b32 v2, v14, v15 offset1:1
	v_add_u32_e32 v2, 0x1048, v73
	ds_write2_b32 v2, v16, v17 offset1:1
	v_add_u32_e32 v2, 0x1450, v73
	ds_write2_b32 v2, v26, v27 offset1:1
	v_add_u32_e32 v2, 0x1458, v73
	ds_write2_b32 v2, v28, v29 offset1:1
	v_add_u32_e32 v2, 0x1860, v73
	ds_write2_b32 v2, v22, v23 offset1:1
	v_add_u32_e32 v2, 0x1868, v73
	ds_write2_b32 v2, v24, v25 offset1:1
	v_add_u32_e32 v2, 0x1c70, v73
	ds_write2_b32 v2, v34, v35 offset1:1
	v_add_u32_e32 v2, 0x1c78, v73
	ds_write2_b32 v2, v36, v37 offset1:1
	v_add_u32_e32 v2, 0x2080, v73
	ds_write2_b32 v2, v30, v31 offset1:1
	v_add_u32_e32 v2, 0x2088, v73
	ds_write2_b32 v2, v32, v33 offset1:1
	v_add_u32_e32 v2, 0x2490, v73
	ds_write2_b32 v2, v42, v43 offset1:1
	v_add_u32_e32 v2, 0x2498, v73
	ds_write2_b32 v2, v44, v45 offset1:1
	v_add_u32_e32 v2, 0x28a0, v73
	ds_write2_b32 v2, v38, v39 offset1:1
	v_add_u32_e32 v2, 0x28a8, v73
	ds_write2_b32 v2, v40, v41 offset1:1
	v_add_u32_e32 v2, 0x2cb0, v73
	ds_write2_b32 v2, v50, v51 offset1:1
	v_add_u32_e32 v2, 0x2cb8, v73
	ds_write2_b32 v2, v52, v53 offset1:1
	v_add_u32_e32 v2, 0x30c0, v73
	ds_write2_b32 v2, v46, v47 offset1:1
	v_add_u32_e32 v2, 0x30c8, v73
	ds_write2_b32 v2, v48, v49 offset1:1
	v_add_u32_e32 v2, 0x34d0, v73
	ds_write2_b32 v2, v58, v59 offset1:1
	v_add_u32_e32 v2, 0x34d8, v73
	ds_write2_b32 v2, v60, v61 offset1:1
	v_add_u32_e32 v2, 0x38e0, v73
	ds_write2_b32 v2, v54, v55 offset1:1
	v_add_u32_e32 v2, 0x38e8, v73
	ds_write2_b32 v2, v56, v57 offset1:1
	v_add_u32_e32 v2, 0x3cf0, v73
	ds_write2_b32 v2, v62, v63 offset1:1
	v_add_u32_e32 v2, 0x3cf8, v73
	ds_write2_b32 v2, v64, v65 offset1:1
	s_waitcnt lgkmcnt(0)
	v_add_u32_e32 v26, 0x400, v88
	ds_read2_b32 v[6:7], v88 offset0:65 offset1:73
	ds_read2_b32 v[8:9], v88 offset1:8
	ds_read2_b32 v[10:11], v88 offset0:130 offset1:138
	ds_read2_b32 v[12:13], v88 offset0:195 offset1:203
	ds_read2_b32 v[16:17], v26 offset0:4 offset1:12
	ds_read2_b32 v[18:19], v26 offset0:69 offset1:77
	ds_read2_b32 v[20:21], v26 offset0:134 offset1:142
	ds_read2_b32 v[22:23], v26 offset0:199 offset1:207
	v_sub_u32_e32 v84, 0, v97
	v_add_u32_e32 v86, v77, v84
	v_ashrrev_i32_e32 v85, 31, v96
	v_ashrrev_i32_e32 v87, 31, v86
	s_waitcnt lgkmcnt(6)
	v_cvt_pk_f16_f32 v2, v8, v6
	s_waitcnt lgkmcnt(4)
	v_cvt_pk_f16_f32 v3, v10, v12
	s_waitcnt lgkmcnt(2)
	v_cvt_pk_f16_f32 v4, v16, v18
	s_waitcnt lgkmcnt(0)
	v_cvt_pk_f16_f32 v5, v20, v22
	v_or_b32_e32 v84, v96, v66
	v_lshl_add_u64 v[14:15], v[86:87], 1, v[82:83]
	v_add_u32_e32 v2, 0x80008, v2
	v_add_u32_e32 v3, 0x80008, v3
	v_add_u32_e32 v4, 0x80008, v4
	v_add_u32_e32 v5, 0x80008, v5
	v_lshlrev_b64 v[24:25], 11, v[84:85]
	v_and_b32_e32 v2, 0xfff0fff0, v2
	v_and_b32_e32 v3, 0xfff0fff0, v3
	v_and_b32_e32 v4, 0xfff0fff0, v4
	v_and_b32_e32 v5, 0xfff0fff0, v5
	v_lshl_add_u64 v[24:25], v[14:15], 0, v[24:25]
	global_store_dwordx4 v[24:25], v[2:5], off nt
	v_or_b32_e32 v84, v96, v68
	v_add_u32_e32 v95, s3, v95
	v_cvt_pk_f16_f32 v2, v9, v7
	v_cvt_pk_f16_f32 v3, v11, v13
	v_cvt_pk_f16_f32 v4, v17, v19
	v_cvt_pk_f16_f32 v5, v21, v23
	v_add_u32_e32 v2, 0x80008, v2
	v_add_u32_e32 v3, 0x80008, v3
	v_add_u32_e32 v4, 0x80008, v4
	v_add_u32_e32 v5, 0x80008, v5
	v_lshlrev_b64 v[6:7], 11, v[84:85]
	v_and_b32_e32 v2, 0xfff0fff0, v2
	v_and_b32_e32 v3, 0xfff0fff0, v3
	v_and_b32_e32 v4, 0xfff0fff0, v4
	v_and_b32_e32 v5, 0xfff0fff0, v5
	v_lshl_add_u64 v[6:7], v[14:15], 0, v[6:7]
	ds_read2_b32 v[8:9], v88 offset0:81 offset1:89
	ds_read2_b32 v[10:11], v88 offset0:16 offset1:24
	ds_read2_b32 v[12:13], v88 offset0:146 offset1:154
	ds_read2_b32 v[16:17], v88 offset0:211 offset1:219
	global_store_dwordx4 v[6:7], v[2:5], off nt
	ds_read2_b32 v[6:7], v26 offset0:20 offset1:28
	ds_read2_b32 v[18:19], v26 offset0:85 offset1:93
	ds_read2_b32 v[20:21], v26 offset0:150 offset1:158
	ds_read2_b32 v[22:23], v26 offset0:215 offset1:223
	s_waitcnt lgkmcnt(6)
	v_cvt_pk_f16_f32 v2, v10, v8
	s_waitcnt lgkmcnt(4)
	v_cvt_pk_f16_f32 v3, v12, v16
	v_or_b32_e32 v84, v96, v70
	s_waitcnt lgkmcnt(2)
	v_cvt_pk_f16_f32 v4, v6, v18
	s_waitcnt lgkmcnt(0)
	v_cvt_pk_f16_f32 v5, v20, v22
	v_add_u32_e32 v2, 0x80008, v2
	v_add_u32_e32 v3, 0x80008, v3
	v_add_u32_e32 v4, 0x80008, v4
	v_add_u32_e32 v5, 0x80008, v5
	v_lshlrev_b64 v[24:25], 11, v[84:85]
	v_and_b32_e32 v2, 0xfff0fff0, v2
	v_and_b32_e32 v3, 0xfff0fff0, v3
	v_and_b32_e32 v4, 0xfff0fff0, v4
	v_and_b32_e32 v5, 0xfff0fff0, v5
	v_lshl_add_u64 v[24:25], v[14:15], 0, v[24:25]
	global_store_dwordx4 v[24:25], v[2:5], off nt
	v_or_b32_e32 v84, v96, v72
	v_cmp_lt_i32_e32 vcc, s16, v95
	v_cvt_pk_f16_f32 v2, v11, v9
	v_cvt_pk_f16_f32 v3, v13, v17
	v_cvt_pk_f16_f32 v4, v7, v19
	v_cvt_pk_f16_f32 v5, v21, v23
	v_add_u32_e32 v2, 0x80008, v2
	v_add_u32_e32 v3, 0x80008, v3
	v_add_u32_e32 v4, 0x80008, v4
	v_add_u32_e32 v5, 0x80008, v5
	v_lshlrev_b64 v[6:7], 11, v[84:85]
	v_and_b32_e32 v2, 0xfff0fff0, v2
	v_and_b32_e32 v3, 0xfff0fff0, v3
	v_and_b32_e32 v4, 0xfff0fff0, v4
	v_and_b32_e32 v5, 0xfff0fff0, v5
	v_lshl_add_u64 v[6:7], v[14:15], 0, v[6:7]
	ds_read2_b32 v[8:9], v88 offset0:32 offset1:40
	ds_read2_b32 v[10:11], v88 offset0:97 offset1:105
	ds_read2_b32 v[12:13], v88 offset0:162 offset1:170
	ds_read2_b32 v[16:17], v88 offset0:227 offset1:235
	global_store_dwordx4 v[6:7], v[2:5], off nt
	ds_read2_b32 v[6:7], v26 offset0:36 offset1:44
	ds_read2_b32 v[18:19], v26 offset0:101 offset1:109
	ds_read2_b32 v[20:21], v26 offset0:166 offset1:174
	ds_read2_b32 v[22:23], v26 offset0:231 offset1:239
	s_waitcnt lgkmcnt(6)
	v_cvt_pk_f16_f32 v2, v8, v10
	s_waitcnt lgkmcnt(4)
	v_cvt_pk_f16_f32 v3, v12, v16
	v_or_b32_e32 v84, v96, v89
	s_waitcnt lgkmcnt(2)
	v_cvt_pk_f16_f32 v4, v6, v18
	s_waitcnt lgkmcnt(0)
	v_cvt_pk_f16_f32 v5, v20, v22
	v_add_u32_e32 v2, 0x80008, v2
	v_add_u32_e32 v3, 0x80008, v3
	v_add_u32_e32 v4, 0x80008, v4
	v_add_u32_e32 v5, 0x80008, v5
	v_lshlrev_b64 v[24:25], 11, v[84:85]
	v_and_b32_e32 v2, 0xfff0fff0, v2
	v_and_b32_e32 v3, 0xfff0fff0, v3
	v_and_b32_e32 v4, 0xfff0fff0, v4
	v_and_b32_e32 v5, 0xfff0fff0, v5
	v_lshl_add_u64 v[24:25], v[14:15], 0, v[24:25]
	global_store_dwordx4 v[24:25], v[2:5], off nt
	v_or_b32_e32 v84, v96, v90
	s_or_b64 s[8:9], vcc, s[8:9]
	v_cvt_pk_f16_f32 v2, v9, v11
	v_cvt_pk_f16_f32 v3, v13, v17
	v_cvt_pk_f16_f32 v4, v7, v19
	v_cvt_pk_f16_f32 v5, v21, v23
	v_add_u32_e32 v2, 0x80008, v2
	v_add_u32_e32 v3, 0x80008, v3
	v_add_u32_e32 v4, 0x80008, v4
	v_add_u32_e32 v5, 0x80008, v5
	v_lshlrev_b64 v[6:7], 11, v[84:85]
	v_and_b32_e32 v2, 0xfff0fff0, v2
	v_and_b32_e32 v3, 0xfff0fff0, v3
	v_and_b32_e32 v4, 0xfff0fff0, v4
	v_and_b32_e32 v5, 0xfff0fff0, v5
	v_lshl_add_u64 v[6:7], v[14:15], 0, v[6:7]
	ds_read2_b32 v[8:9], v88 offset0:48 offset1:56
	ds_read2_b32 v[10:11], v88 offset0:113 offset1:121
	ds_read2_b32 v[12:13], v88 offset0:178 offset1:186
	ds_read2_b32 v[16:17], v88 offset0:243 offset1:251
	global_store_dwordx4 v[6:7], v[2:5], off nt
	ds_read2_b32 v[6:7], v26 offset0:52 offset1:60
	ds_read2_b32 v[18:19], v26 offset0:117 offset1:125
	ds_read2_b32 v[20:21], v26 offset0:182 offset1:190
	ds_read2_b32 v[22:23], v26 offset0:247 offset1:255
	s_waitcnt lgkmcnt(6)
	v_cvt_pk_f16_f32 v2, v8, v10
	s_waitcnt lgkmcnt(4)
	v_cvt_pk_f16_f32 v3, v12, v16
	v_or_b32_e32 v84, v96, v91
	s_waitcnt lgkmcnt(2)
	v_cvt_pk_f16_f32 v4, v6, v18
	s_waitcnt lgkmcnt(0)
	v_cvt_pk_f16_f32 v5, v20, v22
	v_add_u32_e32 v2, 0x80008, v2
	v_add_u32_e32 v3, 0x80008, v3
	v_add_u32_e32 v4, 0x80008, v4
	v_add_u32_e32 v5, 0x80008, v5
	v_lshlrev_b64 v[24:25], 11, v[84:85]
	v_and_b32_e32 v2, 0xfff0fff0, v2
	v_and_b32_e32 v3, 0xfff0fff0, v3
	v_and_b32_e32 v4, 0xfff0fff0, v4
	v_and_b32_e32 v5, 0xfff0fff0, v5
	v_lshl_add_u64 v[24:25], v[14:15], 0, v[24:25]
	global_store_dwordx4 v[24:25], v[2:5], off nt
	v_or_b32_e32 v84, v96, v92
	v_add_u32_e32 v77, s14, v77
	v_cvt_pk_f16_f32 v2, v9, v11
	v_cvt_pk_f16_f32 v3, v13, v17
	v_cvt_pk_f16_f32 v4, v7, v19
	v_cvt_pk_f16_f32 v5, v21, v23
	v_add_u32_e32 v2, 0x80008, v2
	v_add_u32_e32 v3, 0x80008, v3
	v_add_u32_e32 v4, 0x80008, v4
	v_add_u32_e32 v5, 0x80008, v5
	v_lshlrev_b64 v[6:7], 11, v[84:85]
	v_and_b32_e32 v2, 0xfff0fff0, v2
	v_and_b32_e32 v3, 0xfff0fff0, v3
	v_and_b32_e32 v4, 0xfff0fff0, v4
	v_and_b32_e32 v5, 0xfff0fff0, v5
	v_lshl_add_u64 v[6:7], v[14:15], 0, v[6:7]
	global_store_dwordx4 v[6:7], v[2:5], off nt
	s_waitcnt lgkmcnt(0)
	s_andn2_b64 exec, exec, s[8:9]
	s_cbranch_execz .LBB0_85

.LBB0_87:
	s_or_b64 exec, exec, s[14:15]
	s_waitcnt vmcnt(0)
	ds_write2_b32 v73, v2, v3 offset1:1
	ds_write2_b32 v73, v4, v5 offset0:2 offset1:3
	v_add_u32_e32 v2, 0x410, v73
	ds_write2_b32 v2, v10, v11 offset1:1
	v_add_u32_e32 v2, 0x418, v73
	ds_write2_b32 v2, v12, v13 offset1:1
	v_add_u32_e32 v2, 0x820, v73
	ds_write2_b32 v2, v6, v7 offset1:1
	v_add_u32_e32 v2, 0x828, v73
	ds_write2_b32 v2, v8, v9 offset1:1
	v_add_u32_e32 v2, 0xc30, v73
	ds_write2_b32 v2, v18, v19 offset1:1
	v_add_u32_e32 v2, 0xc38, v73
	ds_write2_b32 v2, v20, v21 offset1:1
	v_add_u32_e32 v2, 0x1040, v73
	ds_write2_b32 v2, v14, v15 offset1:1
	v_add_u32_e32 v2, 0x1048, v73
	ds_write2_b32 v2, v16, v17 offset1:1
	v_add_u32_e32 v2, 0x1450, v73
	ds_write2_b32 v2, v26, v27 offset1:1
	v_add_u32_e32 v2, 0x1458, v73
	ds_write2_b32 v2, v28, v29 offset1:1
	v_add_u32_e32 v2, 0x1860, v73
	ds_write2_b32 v2, v22, v23 offset1:1
	v_add_u32_e32 v2, 0x1868, v73
	ds_write2_b32 v2, v24, v25 offset1:1
	v_add_u32_e32 v2, 0x1c70, v73
	ds_write2_b32 v2, v34, v35 offset1:1
	v_add_u32_e32 v2, 0x1c78, v73
	ds_write2_b32 v2, v36, v37 offset1:1
	v_add_u32_e32 v2, 0x2080, v73
	ds_write2_b32 v2, v30, v31 offset1:1
	v_add_u32_e32 v2, 0x2088, v73
	ds_write2_b32 v2, v32, v33 offset1:1
	v_add_u32_e32 v2, 0x2490, v73
	ds_write2_b32 v2, v42, v43 offset1:1
	v_add_u32_e32 v2, 0x2498, v73
	ds_write2_b32 v2, v44, v45 offset1:1
	v_add_u32_e32 v2, 0x28a0, v73
	ds_write2_b32 v2, v38, v39 offset1:1
	v_add_u32_e32 v2, 0x28a8, v73
	ds_write2_b32 v2, v40, v41 offset1:1
	v_add_u32_e32 v2, 0x2cb0, v73
	ds_write2_b32 v2, v50, v51 offset1:1
	v_add_u32_e32 v2, 0x2cb8, v73
	ds_write2_b32 v2, v52, v53 offset1:1
	v_add_u32_e32 v2, 0x30c0, v73
	ds_write2_b32 v2, v46, v47 offset1:1
	v_add_u32_e32 v2, 0x30c8, v73
	ds_write2_b32 v2, v48, v49 offset1:1
	v_add_u32_e32 v2, 0x34d0, v73
	ds_write2_b32 v2, v58, v59 offset1:1
	v_add_u32_e32 v2, 0x34d8, v73
	ds_write2_b32 v2, v60, v61 offset1:1
	v_add_u32_e32 v2, 0x38e0, v73
	ds_write2_b32 v2, v54, v55 offset1:1
	v_add_u32_e32 v2, 0x38e8, v73
	ds_write2_b32 v2, v56, v57 offset1:1
	v_add_u32_e32 v2, 0x3cf0, v73
	ds_write2_b32 v2, v62, v63 offset1:1
	v_add_u32_e32 v2, 0x3cf8, v73
	ds_write2_b32 v2, v64, v65 offset1:1
	s_waitcnt lgkmcnt(0)
	v_add_u32_e32 v26, 0x400, v88
	ds_read2_b32 v[6:7], v88 offset0:65 offset1:73
	ds_read2_b32 v[8:9], v88 offset1:8
	ds_read2_b32 v[10:11], v88 offset0:130 offset1:138
	ds_read2_b32 v[12:13], v88 offset0:195 offset1:203
	ds_read2_b32 v[16:17], v26 offset0:4 offset1:12
	ds_read2_b32 v[18:19], v26 offset0:69 offset1:77
	ds_read2_b32 v[20:21], v26 offset0:134 offset1:142
	ds_read2_b32 v[22:23], v26 offset0:199 offset1:207
	v_lshlrev_b32_e32 v86, 11, v96
	v_sub_u32_e32 v96, v77, v86
	v_ashrrev_i32_e32 v87, 31, v95
	v_ashrrev_i32_e32 v97, 31, v96
	s_waitcnt lgkmcnt(6)
	v_cvt_pk_f16_f32 v2, v8, v6
	s_waitcnt lgkmcnt(4)
	v_cvt_pk_f16_f32 v3, v10, v12
	s_waitcnt lgkmcnt(2)
	v_cvt_pk_f16_f32 v4, v16, v18
	s_waitcnt lgkmcnt(0)
	v_cvt_pk_f16_f32 v5, v20, v22
	v_or_b32_e32 v86, v95, v66
	v_lshl_add_u64 v[14:15], v[96:97], 1, v[82:83]
	v_add_u32_e32 v2, 0x80008, v2
	v_add_u32_e32 v3, 0x80008, v3
	v_add_u32_e32 v4, 0x80008, v4
	v_add_u32_e32 v5, 0x80008, v5
	v_lshlrev_b64 v[24:25], 12, v[86:87]
	v_and_b32_e32 v2, 0xfff0fff0, v2
	v_and_b32_e32 v3, 0xfff0fff0, v3
	v_and_b32_e32 v4, 0xfff0fff0, v4
	v_and_b32_e32 v5, 0xfff0fff0, v5
	v_lshl_add_u64 v[24:25], v[14:15], 0, v[24:25]
	global_store_dwordx4 v[24:25], v[2:5], off nt
	v_or_b32_e32 v86, v95, v68
	v_add_u32_e32 v85, s3, v85
	v_cvt_pk_f16_f32 v2, v9, v7
	v_cvt_pk_f16_f32 v3, v11, v13
	v_cvt_pk_f16_f32 v4, v17, v19
	v_cvt_pk_f16_f32 v5, v21, v23
	v_add_u32_e32 v2, 0x80008, v2
	v_add_u32_e32 v3, 0x80008, v3
	v_add_u32_e32 v4, 0x80008, v4
	v_add_u32_e32 v5, 0x80008, v5
	v_lshlrev_b64 v[6:7], 12, v[86:87]
	v_and_b32_e32 v2, 0xfff0fff0, v2
	v_and_b32_e32 v3, 0xfff0fff0, v3
	v_and_b32_e32 v4, 0xfff0fff0, v4
	v_and_b32_e32 v5, 0xfff0fff0, v5
	v_lshl_add_u64 v[6:7], v[14:15], 0, v[6:7]
	ds_read2_b32 v[8:9], v88 offset0:81 offset1:89
	ds_read2_b32 v[10:11], v88 offset0:16 offset1:24
	ds_read2_b32 v[12:13], v88 offset0:146 offset1:154
	ds_read2_b32 v[16:17], v88 offset0:211 offset1:219
	global_store_dwordx4 v[6:7], v[2:5], off nt
	ds_read2_b32 v[6:7], v26 offset0:20 offset1:28
	ds_read2_b32 v[18:19], v26 offset0:85 offset1:93
	ds_read2_b32 v[20:21], v26 offset0:150 offset1:158
	ds_read2_b32 v[22:23], v26 offset0:215 offset1:223
	s_waitcnt lgkmcnt(6)
	v_cvt_pk_f16_f32 v2, v10, v8
	s_waitcnt lgkmcnt(4)
	v_cvt_pk_f16_f32 v3, v12, v16
	v_or_b32_e32 v86, v95, v70
	s_waitcnt lgkmcnt(2)
	v_cvt_pk_f16_f32 v4, v6, v18
	s_waitcnt lgkmcnt(0)
	v_cvt_pk_f16_f32 v5, v20, v22
	v_add_u32_e32 v2, 0x80008, v2
	v_add_u32_e32 v3, 0x80008, v3
	v_add_u32_e32 v4, 0x80008, v4
	v_add_u32_e32 v5, 0x80008, v5
	v_lshlrev_b64 v[24:25], 12, v[86:87]
	v_and_b32_e32 v2, 0xfff0fff0, v2
	v_and_b32_e32 v3, 0xfff0fff0, v3
	v_and_b32_e32 v4, 0xfff0fff0, v4
	v_and_b32_e32 v5, 0xfff0fff0, v5
	v_lshl_add_u64 v[24:25], v[14:15], 0, v[24:25]
	global_store_dwordx4 v[24:25], v[2:5], off nt
	v_or_b32_e32 v86, v95, v72
	v_cmp_lt_i32_e32 vcc, s21, v85
	v_cvt_pk_f16_f32 v2, v11, v9
	v_cvt_pk_f16_f32 v3, v13, v17
	v_cvt_pk_f16_f32 v4, v7, v19
	v_cvt_pk_f16_f32 v5, v21, v23
	v_add_u32_e32 v2, 0x80008, v2
	v_add_u32_e32 v3, 0x80008, v3
	v_add_u32_e32 v4, 0x80008, v4
	v_add_u32_e32 v5, 0x80008, v5
	v_lshlrev_b64 v[6:7], 12, v[86:87]
	v_and_b32_e32 v2, 0xfff0fff0, v2
	v_and_b32_e32 v3, 0xfff0fff0, v3
	v_and_b32_e32 v4, 0xfff0fff0, v4
	v_and_b32_e32 v5, 0xfff0fff0, v5
	v_lshl_add_u64 v[6:7], v[14:15], 0, v[6:7]
	ds_read2_b32 v[8:9], v88 offset0:32 offset1:40
	ds_read2_b32 v[10:11], v88 offset0:97 offset1:105
	ds_read2_b32 v[12:13], v88 offset0:162 offset1:170
	ds_read2_b32 v[16:17], v88 offset0:227 offset1:235
	global_store_dwordx4 v[6:7], v[2:5], off nt
	ds_read2_b32 v[6:7], v26 offset0:36 offset1:44
	ds_read2_b32 v[18:19], v26 offset0:101 offset1:109
	ds_read2_b32 v[20:21], v26 offset0:166 offset1:174
	ds_read2_b32 v[22:23], v26 offset0:231 offset1:239
	s_waitcnt lgkmcnt(6)
	v_cvt_pk_f16_f32 v2, v8, v10
	s_waitcnt lgkmcnt(4)
	v_cvt_pk_f16_f32 v3, v12, v16
	v_or_b32_e32 v86, v95, v89
	s_waitcnt lgkmcnt(2)
	v_cvt_pk_f16_f32 v4, v6, v18
	s_waitcnt lgkmcnt(0)
	v_cvt_pk_f16_f32 v5, v20, v22
	v_add_u32_e32 v2, 0x80008, v2
	v_add_u32_e32 v3, 0x80008, v3
	v_add_u32_e32 v4, 0x80008, v4
	v_add_u32_e32 v5, 0x80008, v5
	v_lshlrev_b64 v[24:25], 12, v[86:87]
	v_and_b32_e32 v2, 0xfff0fff0, v2
	v_and_b32_e32 v3, 0xfff0fff0, v3
	v_and_b32_e32 v4, 0xfff0fff0, v4
	v_and_b32_e32 v5, 0xfff0fff0, v5
	v_lshl_add_u64 v[24:25], v[14:15], 0, v[24:25]
	global_store_dwordx4 v[24:25], v[2:5], off nt
	v_or_b32_e32 v86, v95, v90
	v_add_u32_e32 v77, s16, v77
	v_cvt_pk_f16_f32 v2, v9, v11
	v_cvt_pk_f16_f32 v3, v13, v17
	v_cvt_pk_f16_f32 v4, v7, v19
	v_cvt_pk_f16_f32 v5, v21, v23
	v_add_u32_e32 v2, 0x80008, v2
	v_add_u32_e32 v3, 0x80008, v3
	v_add_u32_e32 v4, 0x80008, v4
	v_add_u32_e32 v5, 0x80008, v5
	v_lshlrev_b64 v[6:7], 12, v[86:87]
	v_and_b32_e32 v2, 0xfff0fff0, v2
	v_and_b32_e32 v3, 0xfff0fff0, v3
	v_and_b32_e32 v4, 0xfff0fff0, v4
	v_and_b32_e32 v5, 0xfff0fff0, v5
	v_lshl_add_u64 v[6:7], v[14:15], 0, v[6:7]
	ds_read2_b32 v[8:9], v88 offset0:48 offset1:56
	ds_read2_b32 v[10:11], v88 offset0:113 offset1:121
	ds_read2_b32 v[12:13], v88 offset0:178 offset1:186
	ds_read2_b32 v[16:17], v88 offset0:243 offset1:251
	global_store_dwordx4 v[6:7], v[2:5], off nt
	ds_read2_b32 v[6:7], v26 offset0:52 offset1:60
	ds_read2_b32 v[18:19], v26 offset0:117 offset1:125
	ds_read2_b32 v[20:21], v26 offset0:182 offset1:190
	ds_read2_b32 v[22:23], v26 offset0:247 offset1:255
	s_waitcnt lgkmcnt(6)
	v_cvt_pk_f16_f32 v2, v8, v10
	s_waitcnt lgkmcnt(4)
	v_cvt_pk_f16_f32 v3, v12, v16
	v_or_b32_e32 v86, v95, v91
	s_waitcnt lgkmcnt(2)
	v_cvt_pk_f16_f32 v4, v6, v18
	s_waitcnt lgkmcnt(0)
	v_cvt_pk_f16_f32 v5, v20, v22
	v_add_u32_e32 v2, 0x80008, v2
	v_add_u32_e32 v3, 0x80008, v3
	v_add_u32_e32 v4, 0x80008, v4
	v_add_u32_e32 v5, 0x80008, v5
	v_lshlrev_b64 v[24:25], 12, v[86:87]
	v_and_b32_e32 v2, 0xfff0fff0, v2
	v_and_b32_e32 v3, 0xfff0fff0, v3
	v_and_b32_e32 v4, 0xfff0fff0, v4
	v_and_b32_e32 v5, 0xfff0fff0, v5
	v_lshl_add_u64 v[24:25], v[14:15], 0, v[24:25]
	global_store_dwordx4 v[24:25], v[2:5], off nt
	v_or_b32_e32 v86, v95, v92
	s_or_b64 s[12:13], vcc, s[12:13]
	v_cvt_pk_f16_f32 v2, v9, v11
	v_cvt_pk_f16_f32 v3, v13, v17
	v_cvt_pk_f16_f32 v4, v7, v19
	v_cvt_pk_f16_f32 v5, v21, v23
	v_add_u32_e32 v2, 0x80008, v2
	v_add_u32_e32 v3, 0x80008, v3
	v_add_u32_e32 v4, 0x80008, v4
	v_add_u32_e32 v5, 0x80008, v5
	v_lshlrev_b64 v[6:7], 12, v[86:87]
	v_and_b32_e32 v2, 0xfff0fff0, v2
	v_and_b32_e32 v3, 0xfff0fff0, v3
	v_and_b32_e32 v4, 0xfff0fff0, v4
	v_and_b32_e32 v5, 0xfff0fff0, v5
	v_lshl_add_u64 v[6:7], v[14:15], 0, v[6:7]
	global_store_dwordx4 v[6:7], v[2:5], off nt
	s_waitcnt lgkmcnt(0)
	v_add_u32_e32 v84, s18, v84
	s_andn2_b64 exec, exec, s[12:13]
	s_cbranch_execz .LBB0_120

.LBB0_122:
	v_mul_hi_i32 v22, v64, s13
	v_lshrrev_b32_e32 v23, 31, v22
	v_ashrrev_i32_e32 v22, 3, v22
	v_add_u32_e32 v23, v22, v23
	v_mad_u64_u32 v[24:25], s[18:19], v23, s14, v[74:75]
	v_lshlrev_b32_e32 v22, 5, v23
	v_add_u32_e32 v26, v24, v66
	v_ashrrev_i32_e32 v23, 31, v22
	v_ashrrev_i32_e32 v25, 31, v24
	v_ashrrev_i32_e32 v27, 31, v26
	v_add_u32_e32 v78, 8, v26
	v_add_u32_e32 v80, 16, v26
	v_add_u32_e32 v84, 24, v26
	v_add_u32_e32 v96, 40, v26
	v_add_u32_e32 v98, 48, v26
	v_add_u32_e32 v100, 56, v26
	v_add_u32_e32 v102, 64, v26
	v_add_u32_e32 v104, 0x48, v26
	v_add_u32_e32 v106, 0x50, v26
	v_add_u32_e32 v108, 0x58, v26
	v_add_u32_e32 v110, 0x60, v26
	v_add_u32_e32 v112, 0x68, v26
	v_add_u32_e32 v114, 0x70, v26
	v_add_u32_e32 v116, 0x78, v26
	v_or_b32_e32 v65, v22, v66
	v_or_b32_e32 v77, v22, v68
	v_or_b32_e32 v95, v22, v70
	v_or_b32_e32 v120, v22, v72
	v_lshl_add_u64 v[82:83], v[22:23], 2, v[18:19]
	v_add_u32_e32 v86, 32, v26
	v_lshl_add_u64 v[28:29], v[20:21], 0, v[24:25]
	v_lshlrev_b64 v[118:119], 13, v[26:27]
	v_ashrrev_i32_e32 v79, 31, v78
	v_ashrrev_i32_e32 v81, 31, v80
	v_ashrrev_i32_e32 v85, 31, v84
	v_ashrrev_i32_e32 v97, 31, v96
	v_ashrrev_i32_e32 v99, 31, v98
	v_ashrrev_i32_e32 v101, 31, v100
	v_ashrrev_i32_e32 v103, 31, v102
	v_ashrrev_i32_e32 v105, 31, v104
	v_ashrrev_i32_e32 v107, 31, v106
	v_ashrrev_i32_e32 v109, 31, v108
	v_ashrrev_i32_e32 v111, 31, v110
	v_ashrrev_i32_e32 v113, 31, v112
	v_ashrrev_i32_e32 v115, 31, v114
	v_ashrrev_i32_e32 v117, 31, v116
	v_ashrrev_i32_e32 v87, 31, v86
	v_mad_i64_i32 v[22:23], s[18:19], v65, s16, v[28:29]
	v_mad_i64_i32 v[24:25], s[18:19], v77, s16, v[28:29]
	v_mad_i64_i32 v[26:27], s[18:19], v95, s16, v[28:29]
	v_mad_i64_i32 v[28:29], s[18:19], v120, s16, v[28:29]
	v_lshl_add_u64 v[118:119], v[82:83], 0, v[118:119]
	v_lshlrev_b64 v[120:121], 13, v[78:79]
	v_lshlrev_b64 v[122:123], 13, v[80:81]
	v_lshlrev_b64 v[84:85], 13, v[84:85]
	v_lshlrev_b64 v[96:97], 13, v[96:97]
	v_lshlrev_b64 v[98:99], 13, v[98:99]
	v_lshlrev_b64 v[100:101], 13, v[100:101]
	v_lshlrev_b64 v[102:103], 13, v[102:103]
	v_lshlrev_b64 v[104:105], 13, v[104:105]
	v_lshlrev_b64 v[106:107], 13, v[106:107]
	v_lshlrev_b64 v[108:109], 13, v[108:109]
	v_lshlrev_b64 v[110:111], 13, v[110:111]
	v_lshlrev_b64 v[112:113], 13, v[112:113]
	v_lshlrev_b64 v[114:115], 13, v[114:115]
	v_lshlrev_b64 v[116:117], 13, v[116:117]
	v_lshlrev_b64 v[86:87], 13, v[86:87]
	global_load_dwordx4 v[78:81], v[118:119], off nt
	v_lshl_add_u64 v[118:119], v[82:83], 0, v[120:121]
	v_lshl_add_u64 v[120:121], v[82:83], 0, v[122:123]
	v_lshl_add_u64 v[122:123], v[82:83], 0, v[84:85]
	v_lshl_add_u64 v[124:125], v[82:83], 0, v[96:97]
	v_lshl_add_u64 v[126:127], v[82:83], 0, v[98:99]
	v_lshl_add_u64 v[128:129], v[82:83], 0, v[100:101]
	v_lshl_add_u64 v[130:131], v[82:83], 0, v[102:103]
	v_lshl_add_u64 v[132:133], v[82:83], 0, v[104:105]
	v_lshl_add_u64 v[134:135], v[82:83], 0, v[106:107]
	v_lshl_add_u64 v[136:137], v[82:83], 0, v[108:109]
	v_lshl_add_u64 v[138:139], v[82:83], 0, v[110:111]
	v_lshl_add_u64 v[140:141], v[82:83], 0, v[112:113]
	v_lshl_add_u64 v[144:145], v[82:83], 0, v[114:115]
	v_lshl_add_u64 v[148:149], v[82:83], 0, v[116:117]
	v_lshl_add_u64 v[86:87], v[82:83], 0, v[86:87]
	global_load_dwordx4 v[82:85], v[118:119], off nt
	global_load_dwordx4 v[96:99], v[120:121], off nt
	global_load_dwordx4 v[100:103], v[122:123], off nt
	global_load_dwordx4 v[104:107], v[86:87], off nt
	global_load_dwordx4 v[108:111], v[124:125], off nt
	global_load_dwordx4 v[112:115], v[126:127], off nt
	global_load_dwordx4 v[116:119], v[128:129], off nt
	s_nop 0
	global_load_dwordx4 v[120:123], v[130:131], off nt
	global_load_dwordx4 v[124:127], v[132:133], off nt
	s_nop 0
	global_load_dwordx4 v[128:131], v[134:135], off nt
	s_nop 0
	global_load_dwordx4 v[132:135], v[136:137], off nt
	s_nop 0
	global_load_dwordx4 v[136:139], v[138:139], off nt
	s_nop 0
	global_load_dwordx4 v[140:143], v[140:141], off nt
	s_nop 0
	global_load_dwordx4 v[144:147], v[144:145], off nt
	s_nop 0
	global_load_dwordx4 v[148:151], v[148:149], off nt
	s_waitcnt vmcnt(15)
	ds_write2_b32 v30, v78, v79 offset1:1
	ds_write2_b32 v30, v80, v81 offset0:2 offset1:3
	s_waitcnt vmcnt(14)
	ds_write2_b32 v31, v82, v83 offset1:1
	ds_write2_b32 v32, v84, v85 offset1:1
	s_waitcnt vmcnt(13)
	ds_write2_b32 v33, v96, v97 offset1:1
	ds_write2_b32 v34, v98, v99 offset1:1
	s_waitcnt vmcnt(12)
	ds_write2_b32 v35, v100, v101 offset1:1
	ds_write2_b32 v36, v102, v103 offset1:1
	s_waitcnt vmcnt(11)
	ds_write2_b32 v37, v104, v105 offset1:1
	ds_write2_b32 v38, v106, v107 offset1:1
	s_waitcnt vmcnt(10)
	ds_write2_b32 v39, v108, v109 offset1:1
	ds_write2_b32 v40, v110, v111 offset1:1
	s_waitcnt vmcnt(9)
	ds_write2_b32 v41, v112, v113 offset1:1
	ds_write2_b32 v42, v114, v115 offset1:1
	s_waitcnt vmcnt(8)
	ds_write2_b32 v43, v116, v117 offset1:1
	ds_write2_b32 v44, v118, v119 offset1:1
	s_waitcnt vmcnt(7)
	ds_write2_b32 v45, v120, v121 offset1:1
	ds_write2_b32 v46, v122, v123 offset1:1
	s_waitcnt vmcnt(6)
	ds_write2_b32 v47, v124, v125 offset1:1
	ds_write2_b32 v48, v126, v127 offset1:1
	s_waitcnt vmcnt(5)
	ds_write2_b32 v49, v128, v129 offset1:1
	ds_write2_b32 v50, v130, v131 offset1:1
	s_waitcnt vmcnt(4)
	ds_write2_b32 v51, v132, v133 offset1:1
	ds_write2_b32 v52, v134, v135 offset1:1
	s_waitcnt vmcnt(3)
	ds_write2_b32 v53, v136, v137 offset1:1
	ds_write2_b32 v54, v138, v139 offset1:1
	s_waitcnt vmcnt(2)
	ds_write2_b32 v55, v140, v141 offset1:1
	ds_write2_b32 v56, v142, v143 offset1:1
	s_waitcnt vmcnt(1)
	ds_write2_b32 v57, v144, v145 offset1:1
	ds_write2_b32 v58, v146, v147 offset1:1
	s_waitcnt vmcnt(0)
	ds_write2_b32 v59, v148, v149 offset1:1
	ds_write2_b32 v60, v150, v151 offset1:1
	s_waitcnt lgkmcnt(0)
	ds_read2_b32 v[78:79], v75 offset1:8
	ds_read2_b32 v[80:81], v75 offset0:33 offset1:41
	ds_read2_b32 v[82:83], v75 offset0:66 offset1:74
	ds_read2_b32 v[84:85], v75 offset0:99 offset1:107
	ds_read2_b32 v[86:87], v75 offset0:132 offset1:140
	ds_read2_b32 v[96:97], v75 offset0:165 offset1:173
	ds_read2_b32 v[98:99], v75 offset0:198 offset1:206
	ds_read2_b32 v[100:101], v75 offset0:231 offset1:239
	ds_read2_b32 v[102:103], v62 offset0:8 offset1:16
	ds_read2_b32 v[104:105], v62 offset0:41 offset1:49
	ds_read2_b32 v[106:107], v62 offset0:74 offset1:82
	ds_read2_b32 v[108:109], v62 offset0:107 offset1:115
	ds_read2_b32 v[110:111], v62 offset0:140 offset1:148
	ds_read2_b32 v[112:113], v62 offset0:173 offset1:181
	ds_read2_b32 v[114:115], v62 offset0:206 offset1:214
	ds_read2_b32 v[116:117], v62 offset0:239 offset1:247
	ds_read2_b32 v[118:119], v75 offset0:16 offset1:24
	ds_read2_b32 v[120:121], v75 offset0:49 offset1:57
	ds_read2_b32 v[122:123], v75 offset0:82 offset1:90
	ds_read2_b32 v[124:125], v75 offset0:115 offset1:123
	ds_read2_b32 v[126:127], v75 offset0:148 offset1:156
	ds_read2_b32 v[128:129], v75 offset0:181 offset1:189
	ds_read2_b32 v[130:131], v75 offset0:214 offset1:222
	ds_read2_b32 v[132:133], v75 offset0:247 offset1:255
	ds_read2_b32 v[134:135], v62 offset0:24 offset1:32
	ds_read2_b32 v[136:137], v62 offset0:57 offset1:65
	ds_read2_b32 v[138:139], v62 offset0:90 offset1:98
	ds_read2_b32 v[140:141], v62 offset0:123 offset1:131
	ds_read2_b32 v[142:143], v62 offset0:156 offset1:164
	ds_read2_b32 v[144:145], v62 offset0:189 offset1:197
	ds_read2_b32 v[146:147], v62 offset0:222 offset1:230
	ds_read2_b32 v[148:149], v63 offset0:127 offset1:135
	s_waitcnt lgkmcnt(14)
	v_mul_f32_e32 v65, 0x43800000, v78
	v_mul_f32_e32 v77, 0x43800000, v80
	v_mul_f32_e32 v78, 0x43800000, v82
	v_mul_f32_e32 v80, 0x43800000, v84
	v_mul_f32_e32 v82, 0x43800000, v86
	v_mul_f32_e32 v84, 0x43800000, v96
	v_mul_f32_e32 v86, 0x43800000, v98
	v_mul_f32_e32 v95, 0x43800000, v100
	v_mul_f32_e32 v96, 0x43800000, v102
	v_mul_f32_e32 v98, 0x43800000, v104
	v_mul_f32_e32 v100, 0x43800000, v106
	v_mul_f32_e32 v104, 0x43800000, v110
	v_mul_f32_e32 v106, 0x43800000, v112
	v_mov_b32_e32 v2, 0
	v_mov_b32_e32 v3, 0
	v_mov_b32_e32 v4, 0
	v_mov_b32_e32 v5, 0
	v_mul_f32_e32 v79, 0x43800000, v79
	v_mul_f32_e32 v81, 0x43800000, v81
	v_mul_f32_e32 v87, 0x43800000, v87
	v_mul_f32_e32 v97, 0x43800000, v97
	v_mul_f32_e32 v103, 0x43800000, v103
	v_mul_f32_e32 v105, 0x43800000, v105
	v_mul_f32_e32 v111, 0x43800000, v111
	v_mul_f32_e32 v112, 0x43800000, v113
	v_med3_f32 v65, v65, s15, v61
	v_med3_f32 v77, v77, s15, v61
	v_med3_f32 v82, v82, s15, v61
	v_med3_f32 v84, v84, s15, v61
	v_med3_f32 v96, v96, s15, v61
	v_med3_f32 v98, v98, s15, v61
	v_med3_f32 v104, v104, s15, v61
	v_med3_f32 v106, v106, s15, v61
	v_mov_b32_e32 v6, 0
	v_mov_b32_e32 v7, 0
	v_mov_b32_e32 v8, 0
	v_mov_b32_e32 v9, 0
	v_mul_f32_e32 v102, 0x43800000, v108
	v_mul_f32_e32 v108, 0x43800000, v114
	v_mul_f32_e32 v110, 0x43800000, v116
	v_mul_f32_e32 v113, 0x43800000, v115
	v_mul_f32_e32 v114, 0x43800000, v117
	v_mul_f32_e32 v115, 0x43800000, v118
	v_mul_f32_e32 v116, 0x43800000, v120
	s_waitcnt lgkmcnt(13)
	v_mul_f32_e32 v117, 0x43800000, v122
	s_waitcnt lgkmcnt(12)
	v_mul_f32_e32 v118, 0x43800000, v124
	s_waitcnt lgkmcnt(11)
	v_mul_f32_e32 v120, 0x43800000, v126
	s_waitcnt lgkmcnt(10)
	v_mul_f32_e32 v122, 0x43800000, v128
	s_waitcnt lgkmcnt(9)
	v_mul_f32_e32 v124, 0x43800000, v130
	s_waitcnt lgkmcnt(8)
	v_mul_f32_e32 v126, 0x43800000, v132
	s_waitcnt lgkmcnt(7)
	v_mul_f32_e32 v128, 0x43800000, v134
	s_waitcnt lgkmcnt(6)
	v_mul_f32_e32 v130, 0x43800000, v136
	s_waitcnt lgkmcnt(5)
	v_mul_f32_e32 v132, 0x43800000, v138
	s_waitcnt lgkmcnt(3)
	v_mul_f32_e32 v136, 0x43800000, v142
	s_waitcnt lgkmcnt(2)
	v_mul_f32_e32 v138, 0x43800000, v144
	v_med3_f32 v79, v79, s15, v61
	v_med3_f32 v81, v81, s15, v61
	v_med3_f32 v87, v87, s15, v61
	v_med3_f32 v97, v97, s15, v61
	v_med3_f32 v103, v103, s15, v61
	v_med3_f32 v105, v105, s15, v61
	v_med3_f32 v111, v111, s15, v61
	v_med3_f32 v112, v112, s15, v61
	v_cvt_pk_fp8_f32 v2, v65, v77
	v_cvt_pk_fp8_f32 v3, v82, v84
	v_cvt_pk_fp8_f32 v4, v96, v98
	v_cvt_pk_fp8_f32 v5, v104, v106
	v_mov_b32_e32 v10, 0
	v_mov_b32_e32 v11, 0
	v_mov_b32_e32 v12, 0
	v_mov_b32_e32 v13, 0
	v_mul_f32_e32 v119, 0x43800000, v119
	v_mul_f32_e32 v121, 0x43800000, v121
	v_mul_f32_e32 v127, 0x43800000, v127
	v_mul_f32_e32 v129, 0x43800000, v129
	v_mul_f32_e32 v135, 0x43800000, v135
	v_mul_f32_e32 v137, 0x43800000, v137
	v_mul_f32_e32 v143, 0x43800000, v143
	v_mul_f32_e32 v144, 0x43800000, v145
	v_med3_f32 v115, v115, s15, v61
	v_med3_f32 v116, v116, s15, v61
	v_med3_f32 v120, v120, s15, v61
	v_med3_f32 v122, v122, s15, v61
	v_med3_f32 v128, v128, s15, v61
	v_med3_f32 v130, v130, s15, v61
	v_med3_f32 v136, v136, s15, v61
	v_med3_f32 v138, v138, s15, v61
	v_cvt_pk_fp8_f32 v6, v79, v81
	v_cvt_pk_fp8_f32 v7, v87, v97
	v_cvt_pk_fp8_f32 v8, v103, v105
	v_cvt_pk_fp8_f32 v9, v111, v112
	v_mov_b32_e32 v14, 0
	v_mov_b32_e32 v15, 0
	v_mov_b32_e32 v16, 0
	v_mov_b32_e32 v17, 0
	v_med3_f32 v119, v119, s15, v61
	v_med3_f32 v121, v121, s15, v61
	v_med3_f32 v127, v127, s15, v61
	v_med3_f32 v129, v129, s15, v61
	v_med3_f32 v135, v135, s15, v61
	v_med3_f32 v137, v137, s15, v61
	v_med3_f32 v143, v143, s15, v61
	v_med3_f32 v144, v144, s15, v61
	v_cvt_pk_fp8_f32 v10, v115, v116
	v_cvt_pk_fp8_f32 v11, v120, v122
	v_cvt_pk_fp8_f32 v12, v128, v130
	v_cvt_pk_fp8_f32 v13, v136, v138
	v_mul_f32_e32 v83, 0x43800000, v83
	v_mul_f32_e32 v85, 0x43800000, v85
	v_mul_f32_e32 v99, 0x43800000, v99
	v_mul_f32_e32 v101, 0x43800000, v101
	v_mul_f32_e32 v107, 0x43800000, v107
	v_mul_f32_e32 v109, 0x43800000, v109
	v_med3_f32 v78, v78, s15, v61
	v_med3_f32 v80, v80, s15, v61
	v_med3_f32 v86, v86, s15, v61
	v_med3_f32 v95, v95, s15, v61
	v_med3_f32 v100, v100, s15, v61
	v_med3_f32 v102, v102, s15, v61
	v_med3_f32 v108, v108, s15, v61
	v_med3_f32 v110, v110, s15, v61
	v_cvt_pk_fp8_f32 v14, v119, v121
	v_cvt_pk_fp8_f32 v15, v127, v129
	v_cvt_pk_fp8_f32 v16, v135, v137
	v_cvt_pk_fp8_f32 v17, v143, v144
	v_mul_f32_e32 v134, 0x43800000, v140
	s_waitcnt lgkmcnt(1)
	v_mul_f32_e32 v140, 0x43800000, v146
	s_waitcnt lgkmcnt(0)
	v_mul_f32_e32 v142, 0x43800000, v148
	v_med3_f32 v83, v83, s15, v61
	v_med3_f32 v85, v85, s15, v61
	v_med3_f32 v99, v99, s15, v61
	v_med3_f32 v101, v101, s15, v61
	v_med3_f32 v107, v107, s15, v61
	v_med3_f32 v109, v109, s15, v61
	v_med3_f32 v113, v113, s15, v61
	v_med3_f32 v114, v114, s15, v61
	v_cvt_pk_fp8_f32 v2, v78, v80 op_sel:[0,0,1]
	v_cvt_pk_fp8_f32 v3, v86, v95 op_sel:[0,0,1]
	v_cvt_pk_fp8_f32 v4, v100, v102 op_sel:[0,0,1]
	v_cvt_pk_fp8_f32 v5, v108, v110 op_sel:[0,0,1]
	v_mul_f32_e32 v123, 0x43800000, v123
	v_mul_f32_e32 v125, 0x43800000, v125
	v_mul_f32_e32 v131, 0x43800000, v131
	v_mul_f32_e32 v133, 0x43800000, v133
	v_mul_f32_e32 v139, 0x43800000, v139
	v_mul_f32_e32 v141, 0x43800000, v141
	v_mul_f32_e32 v145, 0x43800000, v147
	v_mul_f32_e32 v146, 0x43800000, v149
	v_med3_f32 v117, v117, s15, v61
	v_med3_f32 v118, v118, s15, v61
	v_med3_f32 v124, v124, s15, v61
	v_med3_f32 v126, v126, s15, v61
	v_med3_f32 v132, v132, s15, v61
	v_med3_f32 v134, v134, s15, v61
	v_med3_f32 v140, v140, s15, v61
	v_med3_f32 v142, v142, s15, v61
	v_cvt_pk_fp8_f32 v6, v83, v85 op_sel:[0,0,1]
	v_cvt_pk_fp8_f32 v7, v99, v101 op_sel:[0,0,1]
	v_cvt_pk_fp8_f32 v8, v107, v109 op_sel:[0,0,1]
	v_cvt_pk_fp8_f32 v9, v113, v114 op_sel:[0,0,1]
	v_med3_f32 v123, v123, s15, v61
	v_med3_f32 v125, v125, s15, v61
	v_med3_f32 v131, v131, s15, v61
	v_med3_f32 v133, v133, s15, v61
	v_med3_f32 v139, v139, s15, v61
	v_med3_f32 v141, v141, s15, v61
	v_med3_f32 v145, v145, s15, v61
	v_med3_f32 v146, v146, s15, v61
	v_cvt_pk_fp8_f32 v10, v117, v118 op_sel:[0,0,1]
	v_cvt_pk_fp8_f32 v11, v124, v126 op_sel:[0,0,1]
	v_cvt_pk_fp8_f32 v12, v132, v134 op_sel:[0,0,1]
	v_cvt_pk_fp8_f32 v13, v140, v142 op_sel:[0,0,1]
	v_cvt_pk_fp8_f32 v14, v123, v125 op_sel:[0,0,1]
	v_cvt_pk_fp8_f32 v15, v131, v133 op_sel:[0,0,1]
	v_cvt_pk_fp8_f32 v16, v139, v141 op_sel:[0,0,1]
	v_cvt_pk_fp8_f32 v17, v145, v146 op_sel:[0,0,1]
	global_store_dwordx4 v[22:23], v[2:5], off nt
	global_store_dwordx4 v[24:25], v[6:9], off nt
	global_store_dwordx4 v[26:27], v[10:13], off nt
	global_store_dwordx4 v[28:29], v[14:17], off nt
	v_add_u32_e32 v64, s3, v64
	s_waitcnt lgkmcnt(0)
	v_cmp_lt_i32_e32 vcc, s17, v64
	s_or_b64 s[8:9], vcc, s[8:9]
	v_add_u32_e32 v74, s12, v74
	s_andn2_b64 exec, exec, s[8:9]
	s_cbranch_execnz .LBB0_122
	s_or_b64 exec, exec, s[8:9]
	v_mov_b32_e32 v77, 0
	v_lshl_add_u64 v[2:3], s[58:59], 0, v[76:77]
	s_mov_b64 s[8:9], 0x38100000
	v_lshl_or_b32 v77, s96, 9, v94
	v_lshl_add_u64 v[74:75], v[2:3], 0, s[8:9]
	v_or_b32_e32 v2, v77, v93
	s_movk_i32 s18, 0x1600
	v_mul_lo_u32 v78, v2, s18
	s_lshl_b32 s16, s3, 6
	s_mul_i32 s17, s3, 0x58000
	s_mov_b64 s[12:13], 0
	s_mov_b32 s19, 0xff500000
	s_movk_i32 s21, 0xaff
	v_mov_b32_e32 v80, v78
	v_mov_b32_e32 v79, v77
	v_mov_b32_e32 v81, v69
	s_branch .LBB0_125
.LBB0_124:
	s_or_b64 exec, exec, s[14:15]
	s_waitcnt vmcnt(0)
	ds_write2_b32 v73, v2, v3 offset1:1
	ds_write2_b32 v73, v4, v5 offset0:2 offset1:3
	v_add_u32_e32 v2, 0x410, v73
	ds_write2_b32 v2, v10, v11 offset1:1
	v_add_u32_e32 v2, 0x418, v73
	ds_write2_b32 v2, v12, v13 offset1:1
	v_add_u32_e32 v2, 0x820, v73
	ds_write2_b32 v2, v6, v7 offset1:1
	v_add_u32_e32 v2, 0x828, v73
	ds_write2_b32 v2, v8, v9 offset1:1
	v_add_u32_e32 v2, 0xc30, v73
	ds_write2_b32 v2, v18, v19 offset1:1
	v_add_u32_e32 v2, 0xc38, v73
	ds_write2_b32 v2, v20, v21 offset1:1
	v_add_u32_e32 v2, 0x1040, v73
	ds_write2_b32 v2, v14, v15 offset1:1
	v_add_u32_e32 v2, 0x1048, v73
	ds_write2_b32 v2, v16, v17 offset1:1
	v_add_u32_e32 v2, 0x1450, v73
	ds_write2_b32 v2, v26, v27 offset1:1
	v_add_u32_e32 v2, 0x1458, v73
	ds_write2_b32 v2, v28, v29 offset1:1
	v_add_u32_e32 v2, 0x1860, v73
	ds_write2_b32 v2, v22, v23 offset1:1
	v_add_u32_e32 v2, 0x1868, v73
	ds_write2_b32 v2, v24, v25 offset1:1
	v_add_u32_e32 v2, 0x1c70, v73
	ds_write2_b32 v2, v34, v35 offset1:1
	v_add_u32_e32 v2, 0x1c78, v73
	ds_write2_b32 v2, v36, v37 offset1:1
	v_add_u32_e32 v2, 0x2080, v73
	ds_write2_b32 v2, v30, v31 offset1:1
	v_add_u32_e32 v2, 0x2088, v73
	ds_write2_b32 v2, v32, v33 offset1:1
	v_add_u32_e32 v2, 0x2490, v73
	ds_write2_b32 v2, v42, v43 offset1:1
	v_add_u32_e32 v2, 0x2498, v73
	ds_write2_b32 v2, v44, v45 offset1:1
	v_add_u32_e32 v2, 0x28a0, v73
	ds_write2_b32 v2, v38, v39 offset1:1
	v_add_u32_e32 v2, 0x28a8, v73
	ds_write2_b32 v2, v40, v41 offset1:1
	v_add_u32_e32 v2, 0x2cb0, v73
	ds_write2_b32 v2, v50, v51 offset1:1
	v_add_u32_e32 v2, 0x2cb8, v73
	ds_write2_b32 v2, v52, v53 offset1:1
	v_add_u32_e32 v2, 0x30c0, v73
	ds_write2_b32 v2, v46, v47 offset1:1
	v_add_u32_e32 v2, 0x30c8, v73
	ds_write2_b32 v2, v48, v49 offset1:1
	v_add_u32_e32 v2, 0x34d0, v73
	ds_write2_b32 v2, v58, v59 offset1:1
	v_add_u32_e32 v2, 0x34d8, v73
	ds_write2_b32 v2, v60, v61 offset1:1
	v_add_u32_e32 v2, 0x38e0, v73
	ds_write2_b32 v2, v54, v55 offset1:1
	v_add_u32_e32 v2, 0x38e8, v73
	ds_write2_b32 v2, v56, v57 offset1:1
	v_add_u32_e32 v2, 0x3cf0, v73
	ds_write2_b32 v2, v62, v63 offset1:1
	v_add_u32_e32 v2, 0x3cf8, v73
	ds_write2_b32 v2, v64, v65 offset1:1
	s_waitcnt lgkmcnt(0)
	v_add_u32_e32 v26, 0x400, v88
	v_ashrrev_i32_e32 v82, 1, v84
	ds_read2_b32 v[6:7], v88 offset0:65 offset1:73
	ds_read2_b32 v[8:9], v88 offset1:8
	ds_read2_b32 v[10:11], v88 offset0:130 offset1:138
	ds_read2_b32 v[12:13], v88 offset0:195 offset1:203
	ds_read2_b32 v[16:17], v26 offset0:4 offset1:12
	ds_read2_b32 v[18:19], v26 offset0:69 offset1:77
	ds_read2_b32 v[20:21], v26 offset0:134 offset1:142
	ds_read2_b32 v[22:23], v26 offset0:199 offset1:207
	v_ashrrev_i32_e32 v83, 31, v82
	v_lshlrev_b64 v[82:83], 8, v[82:83]
	v_and_or_b32 v86, v85, 64, v82
	v_lshlrev_b32_e32 v82, 11, v84
	v_sub_u32_e32 v84, v79, v82
	v_ashrrev_i32_e32 v85, 31, v84
	s_waitcnt lgkmcnt(6)
	v_cvt_pk_f16_f32 v2, v8, v6
	s_waitcnt lgkmcnt(4)
	v_cvt_pk_f16_f32 v3, v10, v12
	s_waitcnt lgkmcnt(2)
	v_cvt_pk_f16_f32 v4, v16, v18
	s_waitcnt lgkmcnt(0)
	v_cvt_pk_f16_f32 v5, v20, v22
	v_or_b32_e32 v82, v86, v66
	v_lshl_add_u64 v[14:15], v[84:85], 1, v[74:75]
	v_add_u32_e32 v2, 0x80008, v2
	v_add_u32_e32 v3, 0x80008, v3
	v_add_u32_e32 v4, 0x80008, v4
	v_add_u32_e32 v5, 0x80008, v5
	v_lshlrev_b64 v[24:25], 12, v[82:83]
	v_and_b32_e32 v2, 0xfff0fff0, v2
	v_and_b32_e32 v3, 0xfff0fff0, v3
	v_and_b32_e32 v4, 0xfff0fff0, v4
	v_and_b32_e32 v5, 0xfff0fff0, v5
	v_lshl_add_u64 v[24:25], v[14:15], 0, v[24:25]
	global_store_dwordx4 v[24:25], v[2:5], off nt
	v_or_b32_e32 v82, v86, v68
	v_add_u32_e32 v81, s3, v81
	v_cvt_pk_f16_f32 v2, v9, v7
	v_cvt_pk_f16_f32 v3, v11, v13
	v_cvt_pk_f16_f32 v4, v17, v19
	v_cvt_pk_f16_f32 v5, v21, v23
	v_add_u32_e32 v2, 0x80008, v2
	v_add_u32_e32 v3, 0x80008, v3
	v_add_u32_e32 v4, 0x80008, v4
	v_add_u32_e32 v5, 0x80008, v5
	v_lshlrev_b64 v[6:7], 12, v[82:83]
	v_and_b32_e32 v2, 0xfff0fff0, v2
	v_and_b32_e32 v3, 0xfff0fff0, v3
	v_and_b32_e32 v4, 0xfff0fff0, v4
	v_and_b32_e32 v5, 0xfff0fff0, v5
	v_lshl_add_u64 v[6:7], v[14:15], 0, v[6:7]
	ds_read2_b32 v[8:9], v88 offset0:81 offset1:89
	ds_read2_b32 v[10:11], v88 offset0:16 offset1:24
	ds_read2_b32 v[12:13], v88 offset0:146 offset1:154
	ds_read2_b32 v[16:17], v88 offset0:211 offset1:219
	global_store_dwordx4 v[6:7], v[2:5], off nt
	ds_read2_b32 v[6:7], v26 offset0:20 offset1:28
	ds_read2_b32 v[18:19], v26 offset0:85 offset1:93
	ds_read2_b32 v[20:21], v26 offset0:150 offset1:158
	ds_read2_b32 v[22:23], v26 offset0:215 offset1:223
	s_waitcnt lgkmcnt(6)
	v_cvt_pk_f16_f32 v2, v10, v8
	s_waitcnt lgkmcnt(4)
	v_cvt_pk_f16_f32 v3, v12, v16
	v_or_b32_e32 v82, v86, v70
	s_waitcnt lgkmcnt(2)
	v_cvt_pk_f16_f32 v4, v6, v18
	s_waitcnt lgkmcnt(0)
	v_cvt_pk_f16_f32 v5, v20, v22
	v_add_u32_e32 v2, 0x80008, v2
	v_add_u32_e32 v3, 0x80008, v3
	v_add_u32_e32 v4, 0x80008, v4
	v_add_u32_e32 v5, 0x80008, v5
	v_lshlrev_b64 v[24:25], 12, v[82:83]
	v_and_b32_e32 v2, 0xfff0fff0, v2
	v_and_b32_e32 v3, 0xfff0fff0, v3
	v_and_b32_e32 v4, 0xfff0fff0, v4
	v_and_b32_e32 v5, 0xfff0fff0, v5
	v_lshl_add_u64 v[24:25], v[14:15], 0, v[24:25]
	global_store_dwordx4 v[24:25], v[2:5], off nt
	v_or_b32_e32 v82, v86, v72
	v_cmp_lt_i32_e32 vcc, s21, v81
	v_cvt_pk_f16_f32 v2, v11, v9
	v_cvt_pk_f16_f32 v3, v13, v17
	v_cvt_pk_f16_f32 v4, v7, v19
	v_cvt_pk_f16_f32 v5, v21, v23
	v_add_u32_e32 v2, 0x80008, v2
	v_add_u32_e32 v3, 0x80008, v3
	v_add_u32_e32 v4, 0x80008, v4
	v_add_u32_e32 v5, 0x80008, v5
	v_lshlrev_b64 v[6:7], 12, v[82:83]
	v_and_b32_e32 v2, 0xfff0fff0, v2
	v_and_b32_e32 v3, 0xfff0fff0, v3
	v_and_b32_e32 v4, 0xfff0fff0, v4
	v_and_b32_e32 v5, 0xfff0fff0, v5
	v_lshl_add_u64 v[6:7], v[14:15], 0, v[6:7]
	ds_read2_b32 v[8:9], v88 offset0:32 offset1:40
	ds_read2_b32 v[10:11], v88 offset0:97 offset1:105
	ds_read2_b32 v[12:13], v88 offset0:162 offset1:170
	ds_read2_b32 v[16:17], v88 offset0:227 offset1:235
	global_store_dwordx4 v[6:7], v[2:5], off nt
	ds_read2_b32 v[6:7], v26 offset0:36 offset1:44
	ds_read2_b32 v[18:19], v26 offset0:101 offset1:109
	ds_read2_b32 v[20:21], v26 offset0:166 offset1:174
	ds_read2_b32 v[22:23], v26 offset0:231 offset1:239
	s_waitcnt lgkmcnt(6)
	v_cvt_pk_f16_f32 v2, v8, v10
	s_waitcnt lgkmcnt(4)
	v_cvt_pk_f16_f32 v3, v12, v16
	v_or_b32_e32 v82, v86, v89
	s_waitcnt lgkmcnt(2)
	v_cvt_pk_f16_f32 v4, v6, v18
	s_waitcnt lgkmcnt(0)
	v_cvt_pk_f16_f32 v5, v20, v22
	v_add_u32_e32 v2, 0x80008, v2
	v_add_u32_e32 v3, 0x80008, v3
	v_add_u32_e32 v4, 0x80008, v4
	v_add_u32_e32 v5, 0x80008, v5
	v_lshlrev_b64 v[24:25], 12, v[82:83]
	v_and_b32_e32 v2, 0xfff0fff0, v2
	v_and_b32_e32 v3, 0xfff0fff0, v3
	v_and_b32_e32 v4, 0xfff0fff0, v4
	v_and_b32_e32 v5, 0xfff0fff0, v5
	v_lshl_add_u64 v[24:25], v[14:15], 0, v[24:25]
	global_store_dwordx4 v[24:25], v[2:5], off nt
	v_or_b32_e32 v82, v86, v90
	v_add_u32_e32 v79, s16, v79
	v_cvt_pk_f16_f32 v2, v9, v11
	v_cvt_pk_f16_f32 v3, v13, v17
	v_cvt_pk_f16_f32 v4, v7, v19
	v_cvt_pk_f16_f32 v5, v21, v23
	v_add_u32_e32 v2, 0x80008, v2
	v_add_u32_e32 v3, 0x80008, v3
	v_add_u32_e32 v4, 0x80008, v4
	v_add_u32_e32 v5, 0x80008, v5
	v_lshlrev_b64 v[6:7], 12, v[82:83]
	v_and_b32_e32 v2, 0xfff0fff0, v2
	v_and_b32_e32 v3, 0xfff0fff0, v3
	v_and_b32_e32 v4, 0xfff0fff0, v4
	v_and_b32_e32 v5, 0xfff0fff0, v5
	v_lshl_add_u64 v[6:7], v[14:15], 0, v[6:7]
	ds_read2_b32 v[8:9], v88 offset0:48 offset1:56
	ds_read2_b32 v[10:11], v88 offset0:113 offset1:121
	ds_read2_b32 v[12:13], v88 offset0:178 offset1:186
	ds_read2_b32 v[16:17], v88 offset0:243 offset1:251
	global_store_dwordx4 v[6:7], v[2:5], off nt
	ds_read2_b32 v[6:7], v26 offset0:52 offset1:60
	ds_read2_b32 v[18:19], v26 offset0:117 offset1:125
	ds_read2_b32 v[20:21], v26 offset0:182 offset1:190
	ds_read2_b32 v[22:23], v26 offset0:247 offset1:255
	s_waitcnt lgkmcnt(6)
	v_cvt_pk_f16_f32 v2, v8, v10
	s_waitcnt lgkmcnt(4)
	v_cvt_pk_f16_f32 v3, v12, v16
	v_or_b32_e32 v82, v86, v91
	s_waitcnt lgkmcnt(2)
	v_cvt_pk_f16_f32 v4, v6, v18
	s_waitcnt lgkmcnt(0)
	v_cvt_pk_f16_f32 v5, v20, v22
	v_add_u32_e32 v2, 0x80008, v2
	v_add_u32_e32 v3, 0x80008, v3
	v_add_u32_e32 v4, 0x80008, v4
	v_add_u32_e32 v5, 0x80008, v5
	v_lshlrev_b64 v[24:25], 12, v[82:83]
	v_and_b32_e32 v2, 0xfff0fff0, v2
	v_and_b32_e32 v3, 0xfff0fff0, v3
	v_and_b32_e32 v4, 0xfff0fff0, v4
	v_and_b32_e32 v5, 0xfff0fff0, v5
	v_lshl_add_u64 v[24:25], v[14:15], 0, v[24:25]
	global_store_dwordx4 v[24:25], v[2:5], off nt
	v_or_b32_e32 v82, v86, v92
	s_or_b64 s[12:13], vcc, s[12:13]
	v_cvt_pk_f16_f32 v2, v9, v11
	v_cvt_pk_f16_f32 v3, v13, v17
	v_cvt_pk_f16_f32 v4, v7, v19
	v_cvt_pk_f16_f32 v5, v21, v23
	v_add_u32_e32 v2, 0x80008, v2
	v_add_u32_e32 v3, 0x80008, v3
	v_add_u32_e32 v4, 0x80008, v4
	v_add_u32_e32 v5, 0x80008, v5
	v_lshlrev_b64 v[6:7], 12, v[82:83]
	v_and_b32_e32 v2, 0xfff0fff0, v2
	v_and_b32_e32 v3, 0xfff0fff0, v3
	v_and_b32_e32 v4, 0xfff0fff0, v4
	v_and_b32_e32 v5, 0xfff0fff0, v5
	v_lshl_add_u64 v[6:7], v[14:15], 0, v[6:7]
	global_store_dwordx4 v[6:7], v[2:5], off nt
	s_waitcnt lgkmcnt(0)
	v_add_u32_e32 v80, s17, v80
	s_andn2_b64 exec, exec, s[12:13]
	s_cbranch_execz .LBB0_157

.LBB0_158:
	s_or_b64 exec, exec, s[14:15]
	s_waitcnt vmcnt(0)
	ds_write2_b32 v73, v2, v3 offset1:1
	ds_write2_b32 v73, v4, v5 offset0:2 offset1:3
	v_add_u32_e32 v2, 0x410, v73
	ds_write2_b32 v2, v6, v7 offset1:1
	v_add_u32_e32 v2, 0x418, v73
	ds_write2_b32 v2, v8, v9 offset1:1
	v_add_u32_e32 v2, 0x820, v73
	ds_write2_b32 v2, v14, v15 offset1:1
	v_add_u32_e32 v2, 0x828, v73
	ds_write2_b32 v2, v16, v17 offset1:1
	v_add_u32_e32 v2, 0xc30, v73
	ds_write2_b32 v2, v10, v11 offset1:1
	v_add_u32_e32 v2, 0xc38, v73
	ds_write2_b32 v2, v12, v13 offset1:1
	v_add_u32_e32 v2, 0x1040, v73
	ds_write2_b32 v2, v22, v23 offset1:1
	v_add_u32_e32 v2, 0x1048, v73
	ds_write2_b32 v2, v24, v25 offset1:1
	v_add_u32_e32 v2, 0x1450, v73
	ds_write2_b32 v2, v18, v19 offset1:1
	v_add_u32_e32 v2, 0x1458, v73
	ds_write2_b32 v2, v20, v21 offset1:1
	v_add_u32_e32 v2, 0x1860, v73
	ds_write2_b32 v2, v30, v31 offset1:1
	v_add_u32_e32 v2, 0x1868, v73
	ds_write2_b32 v2, v32, v33 offset1:1
	v_add_u32_e32 v2, 0x1c70, v73
	ds_write2_b32 v2, v26, v27 offset1:1
	v_add_u32_e32 v2, 0x1c78, v73
	ds_write2_b32 v2, v28, v29 offset1:1
	v_add_u32_e32 v2, 0x2080, v73
	ds_write2_b32 v2, v38, v39 offset1:1
	v_add_u32_e32 v2, 0x2088, v73
	ds_write2_b32 v2, v40, v41 offset1:1
	v_add_u32_e32 v2, 0x2490, v73
	ds_write2_b32 v2, v34, v35 offset1:1
	v_add_u32_e32 v2, 0x2498, v73
	ds_write2_b32 v2, v36, v37 offset1:1
	v_add_u32_e32 v2, 0x28a0, v73
	ds_write2_b32 v2, v46, v47 offset1:1
	v_add_u32_e32 v2, 0x28a8, v73
	ds_write2_b32 v2, v48, v49 offset1:1
	v_add_u32_e32 v2, 0x2cb0, v73
	ds_write2_b32 v2, v42, v43 offset1:1
	v_add_u32_e32 v2, 0x2cb8, v73
	ds_write2_b32 v2, v44, v45 offset1:1
	v_add_u32_e32 v2, 0x30c0, v73
	ds_write2_b32 v2, v54, v55 offset1:1
	v_add_u32_e32 v2, 0x30c8, v73
	ds_write2_b32 v2, v56, v57 offset1:1
	v_add_u32_e32 v2, 0x34d0, v73
	ds_write2_b32 v2, v50, v51 offset1:1
	v_add_u32_e32 v2, 0x34d8, v73
	ds_write2_b32 v2, v52, v53 offset1:1
	v_add_u32_e32 v2, 0x38e0, v73
	ds_write2_b32 v2, v62, v63 offset1:1
	v_add_u32_e32 v2, 0x38e8, v73
	ds_write2_b32 v2, v64, v65 offset1:1
	v_add_u32_e32 v2, 0x3cf0, v73
	ds_write2_b32 v2, v58, v59 offset1:1
	v_add_u32_e32 v2, 0x3cf8, v73
	ds_write2_b32 v2, v60, v61 offset1:1
	s_waitcnt lgkmcnt(0)
	v_add_u32_e32 v26, 0x400, v88
	v_ashrrev_i32_e32 v80, 1, v82
	ds_read2_b32 v[6:7], v88 offset0:65 offset1:73
	ds_read2_b32 v[8:9], v88 offset1:8
	ds_read2_b32 v[10:11], v88 offset0:130 offset1:138
	ds_read2_b32 v[12:13], v88 offset0:195 offset1:203
	ds_read2_b32 v[16:17], v26 offset0:4 offset1:12
	ds_read2_b32 v[18:19], v26 offset0:69 offset1:77
	ds_read2_b32 v[20:21], v26 offset0:134 offset1:142
	ds_read2_b32 v[22:23], v26 offset0:199 offset1:207
	v_ashrrev_i32_e32 v81, 31, v80
	v_lshlrev_b64 v[80:81], 8, v[80:81]
	v_and_b32_e32 v83, 64, v83
	v_or3_b32 v84, v80, v83, s21
	v_lshlrev_b32_e32 v80, 11, v82
	v_sub_u32_e32 v82, v77, v80
	v_ashrrev_i32_e32 v83, 31, v82
	s_waitcnt lgkmcnt(6)
	v_cvt_pk_f16_f32 v2, v8, v6
	s_waitcnt lgkmcnt(4)
	v_cvt_pk_f16_f32 v3, v10, v12
	s_waitcnt lgkmcnt(2)
	v_cvt_pk_f16_f32 v4, v16, v18
	s_waitcnt lgkmcnt(0)
	v_cvt_pk_f16_f32 v5, v20, v22
	v_or_b32_e32 v80, v84, v66
	v_lshl_add_u64 v[14:15], v[82:83], 1, v[74:75]
	v_add_u32_e32 v2, 0x80008, v2
	v_add_u32_e32 v3, 0x80008, v3
	v_add_u32_e32 v4, 0x80008, v4
	v_add_u32_e32 v5, 0x80008, v5
	v_lshlrev_b64 v[24:25], 12, v[80:81]
	v_and_b32_e32 v2, 0xfff0fff0, v2
	v_and_b32_e32 v3, 0xfff0fff0, v3
	v_and_b32_e32 v4, 0xfff0fff0, v4
	v_and_b32_e32 v5, 0xfff0fff0, v5
	v_lshl_add_u64 v[24:25], v[14:15], 0, v[24:25]
	global_store_dwordx4 v[24:25], v[2:5], off nt
	v_or_b32_e32 v80, v84, v68
	v_add_u32_e32 v79, s3, v79
	v_cvt_pk_f16_f32 v2, v9, v7
	v_cvt_pk_f16_f32 v3, v11, v13
	v_cvt_pk_f16_f32 v4, v17, v19
	v_cvt_pk_f16_f32 v5, v21, v23
	v_add_u32_e32 v2, 0x80008, v2
	v_add_u32_e32 v3, 0x80008, v3
	v_add_u32_e32 v4, 0x80008, v4
	v_add_u32_e32 v5, 0x80008, v5
	v_lshlrev_b64 v[6:7], 12, v[80:81]
	v_and_b32_e32 v2, 0xfff0fff0, v2
	v_and_b32_e32 v3, 0xfff0fff0, v3
	v_and_b32_e32 v4, 0xfff0fff0, v4
	v_and_b32_e32 v5, 0xfff0fff0, v5
	v_lshl_add_u64 v[6:7], v[14:15], 0, v[6:7]
	ds_read2_b32 v[8:9], v88 offset0:81 offset1:89
	ds_read2_b32 v[10:11], v88 offset0:16 offset1:24
	ds_read2_b32 v[12:13], v88 offset0:146 offset1:154
	ds_read2_b32 v[16:17], v88 offset0:211 offset1:219
	global_store_dwordx4 v[6:7], v[2:5], off nt
	ds_read2_b32 v[6:7], v26 offset0:20 offset1:28
	ds_read2_b32 v[18:19], v26 offset0:85 offset1:93
	ds_read2_b32 v[20:21], v26 offset0:150 offset1:158
	ds_read2_b32 v[22:23], v26 offset0:215 offset1:223
	s_waitcnt lgkmcnt(6)
	v_cvt_pk_f16_f32 v2, v10, v8
	s_waitcnt lgkmcnt(4)
	v_cvt_pk_f16_f32 v3, v12, v16
	v_or_b32_e32 v80, v84, v70
	s_waitcnt lgkmcnt(2)
	v_cvt_pk_f16_f32 v4, v6, v18
	s_waitcnt lgkmcnt(0)
	v_cvt_pk_f16_f32 v5, v20, v22
	v_add_u32_e32 v2, 0x80008, v2
	v_add_u32_e32 v3, 0x80008, v3
	v_add_u32_e32 v4, 0x80008, v4
	v_add_u32_e32 v5, 0x80008, v5
	v_lshlrev_b64 v[24:25], 12, v[80:81]
	v_and_b32_e32 v2, 0xfff0fff0, v2
	v_and_b32_e32 v3, 0xfff0fff0, v3
	v_and_b32_e32 v4, 0xfff0fff0, v4
	v_and_b32_e32 v5, 0xfff0fff0, v5
	v_lshl_add_u64 v[24:25], v[14:15], 0, v[24:25]
	global_store_dwordx4 v[24:25], v[2:5], off nt
	v_or_b32_e32 v80, v84, v72
	v_cmp_lt_i32_e32 vcc, s22, v79
	v_cvt_pk_f16_f32 v2, v11, v9
	v_cvt_pk_f16_f32 v3, v13, v17
	v_cvt_pk_f16_f32 v4, v7, v19
	v_cvt_pk_f16_f32 v5, v21, v23
	v_add_u32_e32 v2, 0x80008, v2
	v_add_u32_e32 v3, 0x80008, v3
	v_add_u32_e32 v4, 0x80008, v4
	v_add_u32_e32 v5, 0x80008, v5
	v_lshlrev_b64 v[6:7], 12, v[80:81]
	v_and_b32_e32 v2, 0xfff0fff0, v2
	v_and_b32_e32 v3, 0xfff0fff0, v3
	v_and_b32_e32 v4, 0xfff0fff0, v4
	v_and_b32_e32 v5, 0xfff0fff0, v5
	v_lshl_add_u64 v[6:7], v[14:15], 0, v[6:7]
	ds_read2_b32 v[8:9], v88 offset0:32 offset1:40
	ds_read2_b32 v[10:11], v88 offset0:97 offset1:105
	ds_read2_b32 v[12:13], v88 offset0:162 offset1:170
	ds_read2_b32 v[16:17], v88 offset0:227 offset1:235
	global_store_dwordx4 v[6:7], v[2:5], off nt
	ds_read2_b32 v[6:7], v26 offset0:36 offset1:44
	ds_read2_b32 v[18:19], v26 offset0:101 offset1:109
	ds_read2_b32 v[20:21], v26 offset0:166 offset1:174
	ds_read2_b32 v[22:23], v26 offset0:231 offset1:239
	s_waitcnt lgkmcnt(6)
	v_cvt_pk_f16_f32 v2, v8, v10
	s_waitcnt lgkmcnt(4)
	v_cvt_pk_f16_f32 v3, v12, v16
	v_or_b32_e32 v80, v84, v89
	s_waitcnt lgkmcnt(2)
	v_cvt_pk_f16_f32 v4, v6, v18
	s_waitcnt lgkmcnt(0)
	v_cvt_pk_f16_f32 v5, v20, v22
	v_add_u32_e32 v2, 0x80008, v2
	v_add_u32_e32 v3, 0x80008, v3
	v_add_u32_e32 v4, 0x80008, v4
	v_add_u32_e32 v5, 0x80008, v5
	v_lshlrev_b64 v[24:25], 12, v[80:81]
	v_and_b32_e32 v2, 0xfff0fff0, v2
	v_and_b32_e32 v3, 0xfff0fff0, v3
	v_and_b32_e32 v4, 0xfff0fff0, v4
	v_and_b32_e32 v5, 0xfff0fff0, v5
	v_lshl_add_u64 v[24:25], v[14:15], 0, v[24:25]
	global_store_dwordx4 v[24:25], v[2:5], off nt
	v_or_b32_e32 v80, v84, v90
	v_add_u32_e32 v77, s16, v77
	v_cvt_pk_f16_f32 v2, v9, v11
	v_cvt_pk_f16_f32 v3, v13, v17
	v_cvt_pk_f16_f32 v4, v7, v19
	v_cvt_pk_f16_f32 v5, v21, v23
	v_add_u32_e32 v2, 0x80008, v2
	v_add_u32_e32 v3, 0x80008, v3
	v_add_u32_e32 v4, 0x80008, v4
	v_add_u32_e32 v5, 0x80008, v5
	v_lshlrev_b64 v[6:7], 12, v[80:81]
	v_and_b32_e32 v2, 0xfff0fff0, v2
	v_and_b32_e32 v3, 0xfff0fff0, v3
	v_and_b32_e32 v4, 0xfff0fff0, v4
	v_and_b32_e32 v5, 0xfff0fff0, v5
	v_lshl_add_u64 v[6:7], v[14:15], 0, v[6:7]
	ds_read2_b32 v[8:9], v88 offset0:48 offset1:56
	ds_read2_b32 v[10:11], v88 offset0:113 offset1:121
	ds_read2_b32 v[12:13], v88 offset0:178 offset1:186
	ds_read2_b32 v[16:17], v88 offset0:243 offset1:251
	global_store_dwordx4 v[6:7], v[2:5], off nt
	ds_read2_b32 v[6:7], v26 offset0:52 offset1:60
	ds_read2_b32 v[18:19], v26 offset0:117 offset1:125
	ds_read2_b32 v[20:21], v26 offset0:182 offset1:190
	ds_read2_b32 v[22:23], v26 offset0:247 offset1:255
	s_waitcnt lgkmcnt(6)
	v_cvt_pk_f16_f32 v2, v8, v10
	s_waitcnt lgkmcnt(4)
	v_cvt_pk_f16_f32 v3, v12, v16
	v_or_b32_e32 v80, v84, v91
	s_waitcnt lgkmcnt(2)
	v_cvt_pk_f16_f32 v4, v6, v18
	s_waitcnt lgkmcnt(0)
	v_cvt_pk_f16_f32 v5, v20, v22
	v_add_u32_e32 v2, 0x80008, v2
	v_add_u32_e32 v3, 0x80008, v3
	v_add_u32_e32 v4, 0x80008, v4
	v_add_u32_e32 v5, 0x80008, v5
	v_lshlrev_b64 v[24:25], 12, v[80:81]
	v_and_b32_e32 v2, 0xfff0fff0, v2
	v_and_b32_e32 v3, 0xfff0fff0, v3
	v_and_b32_e32 v4, 0xfff0fff0, v4
	v_and_b32_e32 v5, 0xfff0fff0, v5
	v_lshl_add_u64 v[24:25], v[14:15], 0, v[24:25]
	global_store_dwordx4 v[24:25], v[2:5], off nt
	v_or_b32_e32 v80, v84, v92
	s_or_b64 s[12:13], vcc, s[12:13]
	v_cvt_pk_f16_f32 v2, v9, v11
	v_cvt_pk_f16_f32 v3, v13, v17
	v_cvt_pk_f16_f32 v4, v7, v19
	v_cvt_pk_f16_f32 v5, v21, v23
	v_add_u32_e32 v2, 0x80008, v2
	v_add_u32_e32 v3, 0x80008, v3
	v_add_u32_e32 v4, 0x80008, v4
	v_add_u32_e32 v5, 0x80008, v5
	v_lshlrev_b64 v[6:7], 12, v[80:81]
	v_and_b32_e32 v2, 0xfff0fff0, v2
	v_and_b32_e32 v3, 0xfff0fff0, v3
	v_and_b32_e32 v4, 0xfff0fff0, v4
	v_and_b32_e32 v5, 0xfff0fff0, v5
	v_lshl_add_u64 v[6:7], v[14:15], 0, v[6:7]
	global_store_dwordx4 v[6:7], v[2:5], off nt
	s_waitcnt lgkmcnt(0)
	v_add_u32_e32 v78, s17, v78
	s_andn2_b64 exec, exec, s[12:13]
	s_cbranch_execz .LBB0_191
